# stack9 + resid_rows loops rescheduled: next-row loads, arithmetic, drain, stores (load latency overlaps the arithmetic; stores overlap the next row); peeled first-iteration header
# speedup vs baseline: 1.0029x; 1.0029x over previous
; #define GAS __attribute__((address_space(1)))
; __device__ __forceinline__ void resid_rows(bf16* X, const bf16* Y, const float* PART, const float* gpost, float* RSv, float* RQv, float* fout, unsigned char* XQv, int m0, int mstep, int lane, int M_end = M) {
;     ...
;         const int mn = m + mstep;
;         if (mn < M) { const GAS v2u* xr = (const GAS v2u*)(X + (size_t)mn * DM) + lane; const GAS v2u* yr = (const GAS v2u*)(Y + (size_t)mn * DM) + lane; np = (lane < 32) ? PART[(size_t)mn * 32 + lane] : 0.f;
; #pragma unroll
;             for (int j = 0; j < 8; ++j) { nx[j] = xr[64 * j]; ny[j] = yr[64 * j]; } }
;     ...
; #pragma unroll
;         for (int j = 0; j < 8; ++j) { cx[j] = nx[j]; cy[j] = ny[j]; }
;         cp = np; m = mn; }
.LBB0_1009:
	s_or_b64 exec, exec, s[48:49]
	v_readlane_b32 s4, v254, 41
	v_readlane_b32 s18, v254, 47
	s_add_u32 s44, s44, s24
	v_readlane_b32 s5, v254, 42
	v_readlane_b32 s19, v254, 48
	s_addc_u32 s45, s45, s25
	v_lshl_add_u64 v[36:37], v[36:37], 0, s[36:37]
	v_lshl_add_u64 v[38:39], v[38:39], 0, s[4:5]
	v_lshl_add_u64 v[40:41], v[40:41], 0, s[18:19]
	v_lshl_add_u64 v[42:43], v[42:43], 0, s[4:5]
	s_andn2_b64 vcc, exec, s[46:47]
	v_mov_b64_e32 v[78:79], v[58:59]
	v_mov_b64_e32 v[82:83], v[56:57]
	v_mov_b64_e32 v[86:87], v[54:55]
	v_mov_b64_e32 v[90:91], v[52:53]
	v_mov_b64_e32 v[94:95], v[50:51]
	v_mov_b64_e32 v[98:99], v[48:49]
	v_mov_b64_e32 v[102:103], v[46:47]
	v_mov_b64_e32 v[106:107], v[44:45]
	v_mov_b64_e32 v[76:77], v[68:69]
	v_mov_b64_e32 v[80:81], v[70:71]
	v_mov_b64_e32 v[84:85], v[72:73]
	v_mov_b64_e32 v[88:89], v[74:75]
	v_mov_b64_e32 v[92:93], v[60:61]
	v_mov_b64_e32 v[96:97], v[62:63]
	v_mov_b64_e32 v[100:101], v[64:65]
	v_mov_b64_e32 v[104:105], v[66:67]
	v_mov_b32_e32 v108, v110
	s_cbranch_vccz .LBB0_1016
	s_add_i32 s0, s0, s94
	s_cmpk_gt_i32 s0, 0x3fff
	s_cselect_b64 s[46:47], -1, 0
	s_and_b64 vcc, exec, s[46:47]
	s_cbranch_vccnz .LBB0_1014
	v_mov_b32_e32 v110, 0
	s_and_saveexec_b64 s[42:43], s[38:39]
	s_cbranch_execz .Lresw0_1013
	v_lshl_add_u64 v[44:45], s[84:85], 0, v[40:41]
	global_load_dword v110, v[44:45], off
.Lresw0_1013:
	s_or_b64 exec, exec, s[42:43]
	v_lshl_add_u64 v[44:45], s[84:85], 0, v[42:43]
	v_add_co_u32_e32 v58, vcc, 0x23800000, v44
	s_nop 1
	v_addc_co_u32_e32 v59, vcc, 0, v45, vcc
	v_add_co_u32_e32 v68, vcc, 0x2b800000, v44
	s_nop 1
	v_addc_co_u32_e32 v69, vcc, 0, v45, vcc
	global_load_dwordx2 v[44:45], v[58:59], off
	global_load_dwordx2 v[46:47], v[58:59], off offset:512
	global_load_dwordx2 v[48:49], v[58:59], off offset:1024
	global_load_dwordx2 v[50:51], v[58:59], off offset:1536
	global_load_dwordx2 v[66:67], v[68:69], off
	global_load_dwordx2 v[64:65], v[68:69], off offset:512
	global_load_dwordx2 v[62:63], v[68:69], off offset:1024
	global_load_dwordx2 v[60:61], v[68:69], off offset:1536
	global_load_dwordx2 v[52:53], v[58:59], off offset:2048
	global_load_dwordx2 v[54:55], v[58:59], off offset:2560
	global_load_dwordx2 v[56:57], v[58:59], off offset:3072
	s_nop 0
	global_load_dwordx2 v[58:59], v[58:59], off offset:3584
	s_nop 0
	global_load_dwordx2 v[74:75], v[68:69], off offset:2048
	global_load_dwordx2 v[72:73], v[68:69], off offset:2560
	global_load_dwordx2 v[70:71], v[68:69], off offset:3072
	s_nop 0
	global_load_dwordx2 v[68:69], v[68:69], off offset:3584
	s_branch .LBB0_1014

; __device__ __forceinline__ void resid_rows(bf16* X, const bf16* Y, const float* PART, const float* gpost, float* RSv, float* RQv, float* fout, unsigned char* XQv, int m0, int mstep, int lane, int M_end = M) {
;     ...
;         const float ps = wave_sum(cp); const float rs1 = 1.f / sqrtf(ps * (1.f / DM) + NORM_EPS);
;         f32x4 v[8]; float s = 0.f;
; #pragma unroll
;         for (int j = 0; j < 8; ++j) { const v2u x = cx[j], y = cy[j];
;             v[j].x = bflo(x.x) + bflo(y.x) * rs1 * g[j].x; v[j].y = bfhi(x.x) + bfhi(y.x) * rs1 * g[j].y; v[j].z = bflo(x.y) + bflo(y.y) * rs1 * g[j].z; v[j].w = bfhi(x.y) + bfhi(y.y) * rs1 * g[j].w;
;             s += (v[j].x * v[j].x + v[j].y * v[j].y) + (v[j].z * v[j].z + v[j].w * v[j].w); }
.LBB0_1014:
	ds_bpermute_b32 v2, v111, v108
	v_lshlrev_b32_e32 v122, 16, v100
	v_and_b32_e32 v123, 0xffff0000, v100
	v_lshlrev_b32_e32 v124, 16, v101
	v_lshlrev_b32_e32 v118, 16, v104
	s_waitcnt lgkmcnt(0)
	v_add_f32_e32 v2, v108, v2
	ds_bpermute_b32 v108, v112, v2
	v_and_b32_e32 v119, 0xffff0000, v104
	v_lshlrev_b32_e32 v104, 16, v105
	v_and_b32_e32 v105, 0xffff0000, v105
	v_and_b32_e32 v109, 0xffff0000, v106
	s_waitcnt lgkmcnt(0)
	v_add_f32_e32 v2, v2, v108
	ds_bpermute_b32 v108, v113, v2
	v_lshlrev_b32_e32 v120, 16, v102
	v_and_b32_e32 v121, 0xffff0000, v102
	v_lshlrev_b32_e32 v102, 16, v103
	v_and_b32_e32 v103, 0xffff0000, v103
	s_waitcnt lgkmcnt(0)
	v_add_f32_e32 v2, v2, v108
	ds_bpermute_b32 v117, v114, v2
	v_lshlrev_b32_e32 v108, 16, v106
	v_lshlrev_b32_e32 v106, 16, v107
	v_and_b32_e32 v107, 0xffff0000, v107
	s_mov_b32 s3, 0x23800000
	s_waitcnt lgkmcnt(0)
	v_add_f32_e32 v2, v2, v117
	ds_bpermute_b32 v117, v115, v2
	s_waitcnt lgkmcnt(0)
	v_add_f32_e32 v2, v2, v117
	ds_bpermute_b32 v117, v116, v2
	s_waitcnt lgkmcnt(0)
	v_add_f32_e32 v2, v2, v117
	v_fmamk_f32 v2, v2, 0x3a000000, v240
	v_mul_f32_e32 v100, 0x4f800000, v2
	v_cmp_gt_f32_e32 vcc, s82, v2
	s_nop 1
	v_cndmask_b32_e32 v2, v2, v100, vcc
	v_sqrt_f32_e32 v100, v2
	s_nop 0
	v_add_u32_e32 v117, -1, v100
	v_add_u32_e32 v125, 1, v100
	v_fma_f32 v126, -v117, v100, v2
	v_fma_f32 v127, -v125, v100, v2
	v_cmp_ge_f32_e64 s[42:43], 0, v126
	s_nop 1
	v_cndmask_b32_e64 v100, v100, v117, s[42:43]
	v_cmp_lt_f32_e64 s[42:43], 0, v127
	s_nop 1
	v_cndmask_b32_e64 v100, v100, v125, s[42:43]
	v_mul_f32_e32 v117, 0x37800000, v100
	v_cndmask_b32_e32 v100, v100, v117, vcc
	v_cmp_class_f32_e32 vcc, v2, v241
	v_and_b32_e32 v125, 0xffff0000, v101
	s_nop 0
	v_cndmask_b32_e32 v2, v100, v2, vcc
	v_div_scale_f32 v100, s[4:5], v2, v2, 1.0
	v_rcp_f32_e32 v117, v100
	v_div_scale_f32 v101, vcc, 1.0, v2, 1.0
	v_fma_f32 v126, -v100, v117, 1.0
	v_fmac_f32_e32 v117, v126, v117
	v_mul_f32_e32 v126, v101, v117
	v_fma_f32 v127, -v100, v126, v101
	v_fmac_f32_e32 v126, v127, v117
	v_fma_f32 v100, -v100, v126, v101
	v_div_fmas_f32 v100, v100, v117, v126
	v_div_fixup_f32 v2, v100, v2, 1.0
	v_pk_mul_f32 v[100:101], v[2:3], v[118:119] op_sel_hi:[0,1]
	v_pk_mul_f32 v[104:105], v[2:3], v[104:105] op_sel_hi:[0,1]
	v_pk_mul_f32 v[118:119], v[2:3], v[122:123] op_sel_hi:[0,1]
	v_pk_fma_f32 v[108:109], v[4:5], v[100:101], v[108:109]
	v_pk_fma_f32 v[106:107], v[6:7], v[104:105], v[106:107]
	v_pk_fma_f32 v[100:101], v[8:9], v[118:119], v[120:121]
	v_pk_mul_f32 v[104:105], v[2:3], v[124:125] op_sel_hi:[0,1]
	v_lshlrev_b32_e32 v118, 16, v96
	v_and_b32_e32 v119, 0xffff0000, v96
	v_pk_fma_f32 v[104:105], v[10:11], v[104:105], v[102:103]
	v_lshlrev_b32_e32 v102, 16, v98
	v_and_b32_e32 v103, 0xffff0000, v98
	v_pk_mul_f32 v[118:119], v[2:3], v[118:119] op_sel_hi:[0,1]
	v_lshlrev_b32_e32 v96, 16, v97
	v_and_b32_e32 v97, 0xffff0000, v97
	v_pk_fma_f32 v[102:103], v[12:13], v[118:119], v[102:103]
	v_lshlrev_b32_e32 v98, 16, v99
	v_and_b32_e32 v99, 0xffff0000, v99
	v_pk_mul_f32 v[96:97], v[2:3], v[96:97] op_sel_hi:[0,1]
	v_lshlrev_b32_e32 v118, 16, v92
	v_and_b32_e32 v119, 0xffff0000, v92
	v_pk_fma_f32 v[98:99], v[14:15], v[96:97], v[98:99]
	v_lshlrev_b32_e32 v96, 16, v94
	v_and_b32_e32 v97, 0xffff0000, v94
	v_pk_mul_f32 v[118:119], v[2:3], v[118:119] op_sel_hi:[0,1]
	v_lshlrev_b32_e32 v92, 16, v93
	v_and_b32_e32 v93, 0xffff0000, v93
	v_pk_fma_f32 v[96:97], v[16:17], v[118:119], v[96:97]
	v_lshlrev_b32_e32 v94, 16, v95
	v_and_b32_e32 v95, 0xffff0000, v95
	v_pk_mul_f32 v[92:93], v[2:3], v[92:93] op_sel_hi:[0,1]
	v_lshlrev_b32_e32 v118, 16, v88
	v_and_b32_e32 v119, 0xffff0000, v88
	v_pk_fma_f32 v[94:95], v[18:19], v[92:93], v[94:95]
	v_lshlrev_b32_e32 v92, 16, v90
	v_and_b32_e32 v93, 0xffff0000, v90
	v_pk_mul_f32 v[118:119], v[2:3], v[118:119] op_sel_hi:[0,1]
	v_lshlrev_b32_e32 v88, 16, v89
	v_and_b32_e32 v89, 0xffff0000, v89
	v_pk_fma_f32 v[92:93], v[20:21], v[118:119], v[92:93]
	v_lshlrev_b32_e32 v90, 16, v91
	v_and_b32_e32 v91, 0xffff0000, v91
	v_pk_mul_f32 v[88:89], v[2:3], v[88:89] op_sel_hi:[0,1]
	v_lshlrev_b32_e32 v118, 16, v84
	v_and_b32_e32 v119, 0xffff0000, v84
	v_pk_fma_f32 v[90:91], v[22:23], v[88:89], v[90:91]
	v_lshlrev_b32_e32 v88, 16, v86
	v_and_b32_e32 v89, 0xffff0000, v86
	v_pk_mul_f32 v[118:119], v[2:3], v[118:119] op_sel_hi:[0,1]
	v_lshlrev_b32_e32 v84, 16, v85
	v_and_b32_e32 v85, 0xffff0000, v85
	v_pk_fma_f32 v[88:89], v[24:25], v[118:119], v[88:89]
	v_lshlrev_b32_e32 v86, 16, v87
	v_and_b32_e32 v87, 0xffff0000, v87
	v_pk_mul_f32 v[84:85], v[2:3], v[84:85] op_sel_hi:[0,1]
	v_lshlrev_b32_e32 v118, 16, v80
	v_and_b32_e32 v119, 0xffff0000, v80
	v_pk_fma_f32 v[86:87], v[26:27], v[84:85], v[86:87]
	v_lshlrev_b32_e32 v84, 16, v82
	v_and_b32_e32 v85, 0xffff0000, v82
	v_pk_mul_f32 v[118:119], v[2:3], v[118:119] op_sel_hi:[0,1]
	v_lshlrev_b32_e32 v80, 16, v81
	v_and_b32_e32 v81, 0xffff0000, v81
	v_pk_fma_f32 v[84:85], v[28:29], v[118:119], v[84:85]
	v_lshlrev_b32_e32 v82, 16, v83
	v_and_b32_e32 v83, 0xffff0000, v83
	v_pk_mul_f32 v[80:81], v[2:3], v[80:81] op_sel_hi:[0,1]
	v_lshlrev_b32_e32 v118, 16, v76
	v_and_b32_e32 v119, 0xffff0000, v76
	v_lshlrev_b32_e32 v76, 16, v77
	v_and_b32_e32 v77, 0xffff0000, v77
	v_pk_fma_f32 v[82:83], v[30:31], v[80:81], v[82:83]
	v_lshlrev_b32_e32 v80, 16, v78
	v_and_b32_e32 v81, 0xffff0000, v78
	v_pk_mul_f32 v[118:119], v[2:3], v[118:119] op_sel_hi:[0,1]
	v_lshlrev_b32_e32 v78, 16, v79
	v_and_b32_e32 v79, 0xffff0000, v79
	v_pk_mul_f32 v[76:77], v[2:3], v[76:77] op_sel_hi:[0,1]
	v_pk_mul_f32 v[120:121], v[100:101], v[100:101]
	v_pk_mul_f32 v[122:123], v[104:105], v[104:105]
; #define GAS __attribute__((address_space(1)))
; __device__ __forceinline__ unsigned pk2(float lo, float hi) { f32x2_t_ v = {lo, hi}; bf16x2_t_ b = __builtin_convertvector(v, bf16x2_t_); return __builtin_bit_cast(unsigned, b); }
; __device__ __forceinline__ float quant_row(const f32x4 (&v)[8], unsigned char* xq, int lane) {
;     float mx = 0.f;
; #pragma unroll
;     for (int j = 0; j < 8; ++j) mx = __builtin_fmaxf(mx, __builtin_fmaxf(__builtin_fmaxf(__builtin_fabsf(v[j].x), __builtin_fabsf(v[j].y)), __builtin_fmaxf(__builtin_fabsf(v[j].z), __builtin_fabsf(v[j].w))));
;     mx = __builtin_fmaxf(wave_max(mx), 1e-20f);
; __device__ __forceinline__ void resid_rows(bf16* X, const bf16* Y, const float* PART, const float* gpost, float* RSv, float* RQv, float* fout, unsigned char* XQv, int m0, int mstep, int lane, int M_end = M) {
;     ...
;             s += (v[j].x * v[j].x + v[j].y * v[j].y) + (v[j].z * v[j].z + v[j].w * v[j].w); }
;         if (fout) { GAS f32x4* xo = (GAS f32x4*)(fout + (size_t)m * DM) + lane;
; #pragma unroll
;             for (int j = 0; j < 8; ++j) xo[64 * j] = v[j]; }
;         else { s = wave_sum(s); GAS v2u* xw = (GAS v2u*)(X + (size_t)m * DM) + lane;
; #pragma unroll
;             for (int j = 0; j < 8; ++j) { v2u w; w.x = pk2(v[j].x, v[j].y); w.y = pk2(v[j].z, v[j].w); xw[64 * j] = w; }
	v_pk_fma_f32 v[80:81], v[32:33], v[118:119], v[80:81]
	v_pk_fma_f32 v[76:77], v[34:35], v[76:77], v[78:79]
	v_pk_mul_f32 v[78:79], v[108:109], v[108:109]
	v_pk_mul_f32 v[118:119], v[106:107], v[106:107]
	v_add_f32_e32 v2, v123, v122
	v_add_f32_e32 v117, v120, v121
	v_add_f32_e32 v2, v117, v2
	v_add_f32_e32 v117, v119, v118
	v_add_f32_e32 v78, v78, v79
	v_pk_mul_f32 v[124:125], v[102:103], v[102:103]
	v_pk_mul_f32 v[126:127], v[98:99], v[98:99]
	v_add_f32_e32 v78, v78, v117
	v_add_f32_e32 v2, v78, v2
	v_add_f32_e32 v78, v127, v126
	v_add_f32_e32 v79, v124, v125
	v_pk_mul_f32 v[128:129], v[96:97], v[96:97]
	v_pk_mul_f32 v[130:131], v[94:95], v[94:95]
	v_add_f32_e32 v78, v79, v78
	v_add_f32_e32 v2, v78, v2
	v_add_f32_e32 v78, v131, v130
	v_add_f32_e32 v79, v128, v129
	v_pk_mul_f32 v[132:133], v[92:93], v[92:93]
	v_pk_mul_f32 v[134:135], v[90:91], v[90:91]
	v_add_f32_e32 v78, v79, v78
	v_add_f32_e32 v2, v78, v2
	v_add_f32_e32 v78, v135, v134
	v_add_f32_e32 v79, v132, v133
	v_pk_mul_f32 v[136:137], v[88:89], v[88:89]
	v_pk_mul_f32 v[138:139], v[86:87], v[86:87]
	v_add_f32_e32 v78, v79, v78
	v_add_f32_e32 v2, v78, v2
	v_add_f32_e32 v78, v139, v138
	v_add_f32_e32 v79, v136, v137
	v_pk_mul_f32 v[140:141], v[84:85], v[84:85]
	v_pk_mul_f32 v[142:143], v[82:83], v[82:83]
	v_add_f32_e32 v78, v79, v78
	v_add_f32_e32 v2, v78, v2
	v_add_f32_e32 v78, v143, v142
	v_add_f32_e32 v79, v140, v141
	v_pk_mul_f32 v[144:145], v[80:81], v[80:81]
	v_pk_mul_f32 v[146:147], v[76:77], v[76:77]
	v_add_f32_e32 v78, v79, v78
	v_add_f32_e32 v2, v78, v2
	v_add_f32_e32 v78, v147, v146
	v_add_f32_e32 v79, v144, v145
	v_add_f32_e32 v78, v79, v78
	v_add_f32_e32 v2, v78, v2
	ds_bpermute_b32 v78, v111, v2
	v_max_f32_e64 v79, |v104|, |v105|
	v_max3_f32 v79, |v100|, |v101|, v79
	v_max_f32_e64 v117, |v94|, |v95|
	v_max3_f32 v117, |v96|, |v97|, v117
	s_waitcnt lgkmcnt(0)
	v_add_f32_e32 v2, v2, v78
	ds_bpermute_b32 v78, v112, v2
	v_lshl_add_u64 v[118:119], s[84:85], 0, v[38:39]
	v_add_co_u32_e32 v118, vcc, s3, v118
	v_cvt_pk_bf16_f32 v120, v108, v109
	s_waitcnt lgkmcnt(0)
	v_add_f32_e32 v2, v2, v78
	ds_bpermute_b32 v78, v113, v2
	v_cvt_pk_bf16_f32 v121, v106, v107
	v_addc_co_u32_e32 v119, vcc, 0, v119, vcc
	s_waitcnt vmcnt(0)
	global_store_dwordx2 v[118:119], v[120:121], off
	s_waitcnt lgkmcnt(0)
	v_add_f32_e32 v2, v2, v78
	ds_bpermute_b32 v78, v114, v2
	v_cvt_pk_bf16_f32 v120, v100, v101
	v_cvt_pk_bf16_f32 v121, v104, v105
	s_mov_b32 s3, 0x1e3ce508
	global_store_dwordx2 v[118:119], v[120:121], off offset:512
	s_waitcnt lgkmcnt(0)
	v_add_f32_e32 v2, v2, v78
	ds_bpermute_b32 v78, v115, v2
	v_cvt_pk_bf16_f32 v120, v102, v103
	v_cvt_pk_bf16_f32 v121, v98, v99
	global_store_dwordx2 v[118:119], v[120:121], off offset:1024
	v_cvt_pk_bf16_f32 v120, v96, v97
	s_waitcnt lgkmcnt(0)
	v_add_f32_e32 v2, v2, v78
	v_max_f32_e64 v78, |v106|, |v107|
	v_max3_f32 v78, |v108|, |v109|, v78
	v_max3_f32 v78, v78, 0, v79
	v_max_f32_e64 v79, |v98|, |v99|
	v_max3_f32 v79, |v102|, |v103|, v79
	v_max3_f32 v78, v78, v79, v117
	v_max_f32_e64 v79, |v90|, |v91|
	v_max_f32_e64 v117, |v86|, |v87|
	v_max3_f32 v79, |v92|, |v93|, v79
	v_max3_f32 v117, |v88|, |v89|, v117
	v_max3_f32 v78, v78, v79, v117
	v_max_f32_e64 v79, |v82|, |v83|
	v_max_f32_e64 v117, |v76|, |v77|
	v_max3_f32 v79, |v84|, |v85|, v79
	v_max3_f32 v117, |v80|, |v81|, v117
	v_max3_f32 v79, v78, v79, v117
	ds_bpermute_b32 v117, v111, v79
	v_cvt_pk_bf16_f32 v121, v94, v95
	global_store_dwordx2 v[118:119], v[120:121], off offset:1536
	v_cvt_pk_bf16_f32 v120, v92, v93
	v_cvt_pk_bf16_f32 v121, v90, v91
	s_waitcnt lgkmcnt(0)
	v_max_f32_e32 v117, v117, v117
	v_max_f32_e32 v79, v79, v117
	ds_bpermute_b32 v117, v112, v79
	global_store_dwordx2 v[118:119], v[120:121], off offset:2048
	v_cvt_pk_bf16_f32 v120, v88, v89
	v_cvt_pk_bf16_f32 v121, v86, v87
	global_store_dwordx2 v[118:119], v[120:121], off offset:2560
	s_waitcnt lgkmcnt(0)
	v_max_f32_e32 v117, v117, v117
	v_max_f32_e32 v79, v79, v117
	ds_bpermute_b32 v117, v113, v79
	v_cvt_pk_bf16_f32 v120, v84, v85
	v_cvt_pk_bf16_f32 v121, v82, v83
	global_store_dwordx2 v[118:119], v[120:121], off offset:3072
	v_cvt_pk_bf16_f32 v120, v80, v81
	s_waitcnt lgkmcnt(0)
	v_max_f32_e32 v117, v117, v117
	v_max_f32_e32 v79, v79, v117
	ds_bpermute_b32 v117, v114, v79
	v_cvt_pk_bf16_f32 v121, v76, v77
	global_store_dwordx2 v[118:119], v[120:121], off offset:3584
	ds_bpermute_b32 v78, v116, v2
	s_waitcnt lgkmcnt(1)
	v_max_f32_e32 v117, v117, v117
	v_max_f32_e32 v79, v79, v117
	ds_bpermute_b32 v117, v115, v79
	s_waitcnt lgkmcnt(0)
	v_max_f32_e32 v117, v117, v117
	v_max_f32_e32 v79, v79, v117
	ds_bpermute_b32 v117, v116, v79
	s_waitcnt lgkmcnt(0)
; #define GAS __attribute__((address_space(1)))
; __device__ __forceinline__ float quant_row(const f32x4 (&v)[8], unsigned char* xq, int lane) {
;     ...
;     const float q = 127.0f / mx;
;     GAS unsigned* o4 = (GAS unsigned*)xq + lane;
; #pragma unroll
;     for (int j = 0; j < 8; ++j) o4[64 * j] = q4(v[j], q);
;     return mx * (1.0f / 127.0f);
; __device__ __forceinline__ void resid_rows(bf16* X, const bf16* Y, const float* PART, const float* gpost, float* RSv, float* RQv, float* fout, unsigned char* XQv, int m0, int mstep, int lane, int M_end = M) {
;     ...
;             const float dq = quant_row(v, XQv + (size_t)m * DM, lane);
;             if (lane == 0) { const float r = 1.f / sqrtf(s * (1.f / DM) + NORM_EPS); RSv[m] = r; RQv[m] = r * dq; } }
	v_max3_f32 v79, v79, v117, s3
	s_mov_b32 s3, 0x42fe0000
	v_div_scale_f32 v117, s[4:5], v79, v79, s3
	v_rcp_f32_e32 v122, v117
	s_nop 0
	v_fma_f32 v118, -v117, v122, 1.0
	v_fmac_f32_e32 v122, v118, v122
	v_div_scale_f32 v118, vcc, s3, v79, s3
	v_mul_f32_e32 v119, v118, v122
	v_fma_f32 v120, -v117, v119, v118
	v_fmac_f32_e32 v119, v120, v122
	v_fma_f32 v117, -v117, v119, v118
	v_div_fmas_f32 v117, v117, v122, v119
	v_div_fixup_f32 v117, v117, v79, s3
	v_mul_f32_e32 v109, v109, v117
	v_mul_f32_e32 v108, v108, v117
	v_rndne_f32_e32 v109, v109
	v_mul_f32_e32 v106, v106, v117
	v_mul_f32_e32 v107, v107, v117
	v_mul_f32_e32 v101, v101, v117
	v_rndne_f32_e32 v108, v108
	v_cvt_i32_f32_e32 v109, v109
	v_rndne_f32_e32 v106, v106
	v_rndne_f32_e32 v107, v107
	v_mul_f32_e32 v100, v100, v117
	v_rndne_f32_e32 v101, v101
	v_mul_f32_e32 v104, v104, v117
	v_mul_f32_e32 v105, v105, v117
	v_cvt_i32_f32_e32 v108, v108
	v_cvt_i32_f32_sdwa v106, v106 dst_sel:WORD_1 dst_unused:UNUSED_PAD src0_sel:DWORD
	v_cvt_i32_f32_e32 v107, v107
	v_rndne_f32_e32 v100, v100
	v_cvt_i32_f32_e32 v101, v101
	v_rndne_f32_e32 v104, v104
	v_rndne_f32_e32 v105, v105
	v_cvt_i32_f32_e32 v100, v100
	v_cvt_i32_f32_sdwa v104, v104 dst_sel:WORD_1 dst_unused:UNUSED_PAD src0_sel:DWORD
	v_cvt_i32_f32_e32 v105, v105
	v_lshlrev_b32_e32 v109, 8, v109
	v_lshl_add_u64 v[118:119], s[84:85], 0, v[36:37]
	v_and_b32_e32 v109, 0xff00, v109
	v_and_b32_e32 v106, 0xff0000, v106
	v_perm_b32 v107, v107, v108, s17
	s_mov_b32 s3, 0x8800000
	v_lshlrev_b32_e32 v101, 8, v101
	v_or3_b32 v108, v107, v109, v106
	v_add_co_u32_e32 v106, vcc, s3, v118
	v_and_b32_e32 v101, 0xff00, v101
	v_and_b32_e32 v104, 0xff0000, v104
	v_perm_b32 v100, v105, v100, s17
	v_addc_co_u32_e32 v107, vcc, 0, v119, vcc
	v_or3_b32 v100, v100, v101, v104
	v_mul_f32_e32 v101, v103, v117
	v_mul_f32_e32 v97, v97, v117
	v_mul_f32_e32 v93, v93, v117
	v_mul_f32_e32 v89, v89, v117
	v_mul_f32_e32 v85, v85, v117
	v_mul_f32_e32 v81, v81, v117
	global_store_dword v[106:107], v100, off offset:256
	v_mul_f32_e32 v100, v102, v117
	v_rndne_f32_e32 v101, v101
	v_mul_f32_e32 v98, v98, v117
	v_mul_f32_e32 v99, v99, v117
	v_mul_f32_e32 v96, v96, v117
	v_rndne_f32_e32 v97, v97
	v_mul_f32_e32 v94, v94, v117
	v_mul_f32_e32 v95, v95, v117
	v_mul_f32_e32 v92, v92, v117
	v_rndne_f32_e32 v93, v93
	v_mul_f32_e32 v90, v90, v117
	v_mul_f32_e32 v91, v91, v117
	v_mul_f32_e32 v88, v88, v117
	v_rndne_f32_e32 v89, v89
	v_mul_f32_e32 v86, v86, v117
	v_mul_f32_e32 v87, v87, v117
	v_mul_f32_e32 v84, v84, v117
	v_rndne_f32_e32 v85, v85
	v_mul_f32_e32 v82, v82, v117
	v_mul_f32_e32 v83, v83, v117
	v_mul_f32_e32 v80, v80, v117
	v_rndne_f32_e32 v81, v81
	v_mul_f32_e32 v76, v76, v117
	v_mul_f32_e32 v77, v77, v117
	v_rndne_f32_e32 v100, v100
	v_cvt_i32_f32_e32 v101, v101
	v_rndne_f32_e32 v98, v98
	v_rndne_f32_e32 v99, v99
	v_rndne_f32_e32 v96, v96
	v_cvt_i32_f32_e32 v97, v97
	v_rndne_f32_e32 v94, v94
	v_rndne_f32_e32 v95, v95
	v_rndne_f32_e32 v92, v92
	v_cvt_i32_f32_e32 v93, v93
	v_rndne_f32_e32 v90, v90
	v_rndne_f32_e32 v91, v91
	v_rndne_f32_e32 v88, v88
	v_cvt_i32_f32_e32 v89, v89
	v_rndne_f32_e32 v86, v86
	v_rndne_f32_e32 v87, v87
	v_rndne_f32_e32 v84, v84
	v_cvt_i32_f32_e32 v85, v85
	v_rndne_f32_e32 v82, v82
	v_rndne_f32_e32 v83, v83
	v_rndne_f32_e32 v80, v80
	v_cvt_i32_f32_e32 v81, v81
	v_rndne_f32_e32 v76, v76
	v_rndne_f32_e32 v77, v77
	v_cvt_i32_f32_e32 v100, v100
	v_cvt_i32_f32_sdwa v98, v98 dst_sel:WORD_1 dst_unused:UNUSED_PAD src0_sel:DWORD
	v_cvt_i32_f32_e32 v99, v99
	v_cvt_i32_f32_e32 v96, v96
	v_cvt_i32_f32_sdwa v94, v94 dst_sel:WORD_1 dst_unused:UNUSED_PAD src0_sel:DWORD
	v_cvt_i32_f32_e32 v95, v95
	v_cvt_i32_f32_e32 v92, v92
	v_cvt_i32_f32_sdwa v90, v90 dst_sel:WORD_1 dst_unused:UNUSED_PAD src0_sel:DWORD
	v_cvt_i32_f32_e32 v91, v91
	v_cvt_i32_f32_e32 v88, v88
	v_cvt_i32_f32_sdwa v86, v86 dst_sel:WORD_1 dst_unused:UNUSED_PAD src0_sel:DWORD
	v_cvt_i32_f32_e32 v87, v87
	v_cvt_i32_f32_e32 v84, v84
	v_cvt_i32_f32_sdwa v82, v82 dst_sel:WORD_1 dst_unused:UNUSED_PAD src0_sel:DWORD
	v_cvt_i32_f32_e32 v83, v83
	v_cvt_i32_f32_e32 v80, v80
	v_cvt_i32_f32_sdwa v76, v76 dst_sel:WORD_1 dst_unused:UNUSED_PAD src0_sel:DWORD
	v_cvt_i32_f32_e32 v77, v77
	v_lshlrev_b32_e32 v101, 8, v101
	v_lshlrev_b32_e32 v97, 8, v97
	v_lshlrev_b32_e32 v93, 8, v93
	v_lshlrev_b32_e32 v89, 8, v89
	v_lshlrev_b32_e32 v85, 8, v85
	v_lshlrev_b32_e32 v81, 8, v81
	v_and_b32_e32 v101, 0xff00, v101
	v_and_b32_e32 v98, 0xff0000, v98
	v_perm_b32 v99, v99, v100, s17
	v_and_b32_e32 v97, 0xff00, v97
	v_and_b32_e32 v94, 0xff0000, v94
	v_perm_b32 v95, v95, v96, s17
	v_and_b32_e32 v93, 0xff00, v93
	v_and_b32_e32 v90, 0xff0000, v90
	v_perm_b32 v91, v91, v92, s17
	v_and_b32_e32 v89, 0xff00, v89
	v_and_b32_e32 v86, 0xff0000, v86
	v_perm_b32 v87, v87, v88, s17
	v_and_b32_e32 v85, 0xff00, v85
	v_and_b32_e32 v82, 0xff0000, v82
	v_perm_b32 v83, v83, v84, s17
	v_and_b32_e32 v81, 0xff00, v81
	v_and_b32_e32 v76, 0xff0000, v76
	v_perm_b32 v77, v77, v80, s17
	v_or3_b32 v98, v99, v101, v98
	v_or3_b32 v94, v95, v97, v94
	v_or3_b32 v90, v91, v93, v90
	v_or3_b32 v86, v87, v89, v86
	v_or3_b32 v82, v83, v85, v82
	v_or3_b32 v76, v77, v81, v76
	global_store_dword v[106:107], v108, off
	global_store_dword v[106:107], v98, off offset:512
	global_store_dword v[106:107], v94, off offset:768
	global_store_dword v[106:107], v90, off offset:1024
	global_store_dword v[106:107], v86, off offset:1280
	global_store_dword v[106:107], v82, off offset:1536
	global_store_dword v[106:107], v76, off offset:1792
	s_and_saveexec_b64 s[48:49], s[40:41]
	s_cbranch_execz .LBB0_1009
	v_add_f32_e32 v2, v2, v78
	v_fmamk_f32 v2, v2, 0x3a000000, v240
	v_mul_f32_e32 v76, 0x4f800000, v2
	v_cmp_gt_f32_e32 vcc, s82, v2
	s_nop 1
	v_cndmask_b32_e32 v2, v2, v76, vcc
	v_sqrt_f32_e32 v76, v2
	s_nop 0
	v_add_u32_e32 v77, -1, v76
	v_fma_f32 v80, -v77, v76, v2
	v_add_u32_e32 v78, 1, v76
	v_cmp_ge_f32_e64 s[42:43], 0, v80
	s_nop 1
	v_cndmask_b32_e64 v77, v76, v77, s[42:43]
	v_fma_f32 v76, -v78, v76, v2
	v_cmp_lt_f32_e64 s[42:43], 0, v76
	s_nop 1
	v_cndmask_b32_e64 v76, v77, v78, s[42:43]
	v_mul_f32_e32 v77, 0x37800000, v76
	v_cndmask_b32_e32 v76, v76, v77, vcc
	v_cmp_class_f32_e32 vcc, v2, v241
	v_mul_f32_e32 v78, 0x3c010204, v79
	s_nop 0
	v_cndmask_b32_e32 v2, v76, v2, vcc
	v_div_scale_f32 v76, s[4:5], v2, v2, 1.0
	v_rcp_f32_e32 v77, v76
	s_add_u32 s4, s84, s44
	s_addc_u32 s5, s85, s45
	v_fma_f32 v79, -v76, v77, 1.0
	v_fmac_f32_e32 v77, v79, v77
	v_div_scale_f32 v79, vcc, 1.0, v2, 1.0
	v_mul_f32_e32 v80, v79, v77
	v_fma_f32 v81, -v76, v80, v79
	v_fmac_f32_e32 v80, v81, v77
	v_fma_f32 v76, -v76, v80, v79
	v_div_fmas_f32 v76, v76, v77, v80
	v_div_fixup_f32 v2, v76, v2, 1.0
	global_store_dword v236, v2, s[4:5]
	v_mul_f32_e32 v2, v78, v2
	global_store_dword v237, v2, s[4:5]
	s_branch .LBB0_1009

; #define GAS __attribute__((address_space(1)))
; __device__ __forceinline__ void resid_rows(bf16* X, const bf16* Y, const float* PART, const float* gpost, float* RSv, float* RQv, float* fout, unsigned char* XQv, int m0, int mstep, int lane, int M_end = M) {
;     ...
;         const int mn = m + mstep;
;         if (mn < M) { const GAS v2u* xr = (const GAS v2u*)(X + (size_t)mn * DM) + lane; const GAS v2u* yr = (const GAS v2u*)(Y + (size_t)mn * DM) + lane; np = (lane < 32) ? PART[(size_t)mn * 32 + lane] : 0.f;
;     ...
; #pragma unroll
;         for (int j = 0; j < 8; ++j) { cx[j] = nx[j]; cy[j] = ny[j]; }
;         cp = np; m = mn; }
.LBB0_1022:
	s_or_b64 exec, exec, s[48:49]
	s_mov_b64 s[4:5], 0x80000
	s_add_u32 s44, s44, 0x400
	v_lshl_add_u64 v[36:37], v[36:37], 0, s[4:5]
	s_mov_b64 s[4:5], 0x100000
	s_mov_b64 s[18:19], 0x8000
	s_addc_u32 s45, s45, 0
	v_lshl_add_u64 v[38:39], v[38:39], 0, s[4:5]
	v_lshl_add_u64 v[40:41], v[40:41], 0, s[18:19]
	v_lshl_add_u64 v[42:43], v[42:43], 0, s[4:5]
	s_and_b64 vcc, exec, s[46:47]
	v_mov_b64_e32 v[78:79], v[58:59]
	v_mov_b64_e32 v[82:83], v[56:57]
	v_mov_b64_e32 v[86:87], v[54:55]
	v_mov_b64_e32 v[90:91], v[52:53]
	v_mov_b64_e32 v[94:95], v[50:51]
	v_mov_b64_e32 v[98:99], v[48:49]
	v_mov_b64_e32 v[102:103], v[46:47]
	v_mov_b64_e32 v[106:107], v[44:45]
	v_mov_b64_e32 v[76:77], v[68:69]
	v_mov_b64_e32 v[80:81], v[70:71]
	v_mov_b64_e32 v[84:85], v[72:73]
	v_mov_b64_e32 v[88:89], v[74:75]
	v_mov_b64_e32 v[92:93], v[60:61]
	v_mov_b64_e32 v[96:97], v[62:63]
	v_mov_b64_e32 v[100:101], v[64:65]
	v_mov_b64_e32 v[104:105], v[66:67]
	v_mov_b32_e32 v108, v110
	s_cbranch_vccnz .LBB0_1029
	s_addk_i32 s0, 0x100
	v_readlane_b32 s3, v253, 35
	s_cmp_ge_i32 s0, s3
	s_cselect_b64 s[46:47], -1, 0
	s_and_b64 vcc, exec, s[46:47]
	s_cbranch_vccnz .LBB0_1027
	v_mov_b32_e32 v110, 0
	s_and_saveexec_b64 s[42:43], s[38:39]
	s_cbranch_execz .Lresw1_1026
	v_lshl_add_u64 v[44:45], s[84:85], 0, v[40:41]
	global_load_dword v110, v[44:45], off

; __device__ __forceinline__ void resid_rows(bf16* X, const bf16* Y, const float* PART, const float* gpost, float* RSv, float* RQv, float* fout, unsigned char* XQv, int m0, int mstep, int lane, int M_end = M) {
;     ...
;         const float ps = wave_sum(cp); const float rs1 = 1.f / sqrtf(ps * (1.f / DM) + NORM_EPS);
;         f32x4 v[8]; float s = 0.f;
; #pragma unroll
;         for (int j = 0; j < 8; ++j) { const v2u x = cx[j], y = cy[j];
;             v[j].x = bflo(x.x) + bflo(y.x) * rs1 * g[j].x; v[j].y = bfhi(x.x) + bfhi(y.x) * rs1 * g[j].y; v[j].z = bflo(x.y) + bflo(y.y) * rs1 * g[j].z; v[j].w = bfhi(x.y) + bfhi(y.y) * rs1 * g[j].w;
;             s += (v[j].x * v[j].x + v[j].y * v[j].y) + (v[j].z * v[j].z + v[j].w * v[j].w); }
.LBB0_1027:
	ds_bpermute_b32 v1, v111, v108
	v_lshlrev_b32_e32 v122, 16, v100
	v_and_b32_e32 v123, 0xffff0000, v100
	v_lshlrev_b32_e32 v124, 16, v101
	v_lshlrev_b32_e32 v118, 16, v104
	s_waitcnt lgkmcnt(0)
	v_add_f32_e32 v1, v108, v1
	ds_bpermute_b32 v2, v112, v1
	v_and_b32_e32 v119, 0xffff0000, v104
	v_lshlrev_b32_e32 v104, 16, v105
	v_and_b32_e32 v105, 0xffff0000, v105
	v_lshlrev_b32_e32 v108, 16, v106
	s_waitcnt lgkmcnt(0)
	v_add_f32_e32 v1, v1, v2
	ds_bpermute_b32 v2, v113, v1
	v_and_b32_e32 v109, 0xffff0000, v106
	v_lshlrev_b32_e32 v106, 16, v107
	v_and_b32_e32 v107, 0xffff0000, v107
	v_lshlrev_b32_e32 v120, 16, v102
	s_waitcnt lgkmcnt(0)
	v_add_f32_e32 v1, v1, v2
	ds_bpermute_b32 v2, v114, v1
	v_and_b32_e32 v121, 0xffff0000, v102
	v_lshlrev_b32_e32 v102, 16, v103
	v_and_b32_e32 v103, 0xffff0000, v103
	s_mov_b32 s3, 0x23800000
	s_waitcnt lgkmcnt(0)
	v_add_f32_e32 v1, v1, v2
	ds_bpermute_b32 v2, v115, v1
	s_waitcnt lgkmcnt(0)
	v_add_f32_e32 v1, v1, v2
	ds_bpermute_b32 v2, v116, v1
	s_waitcnt lgkmcnt(0)
	v_add_f32_e32 v1, v1, v2
	v_fmamk_f32 v1, v1, 0x3a000000, v240
	v_mul_f32_e32 v2, 0x4f800000, v1
	v_cmp_gt_f32_e32 vcc, s82, v1
	s_nop 1
	v_cndmask_b32_e32 v1, v1, v2, vcc
	v_sqrt_f32_e32 v2, v1
	s_nop 0
	v_add_u32_e32 v100, -1, v2
	v_add_u32_e32 v117, 1, v2
	v_fma_f32 v125, -v100, v2, v1
	v_fma_f32 v126, -v117, v2, v1
	v_cmp_ge_f32_e64 s[42:43], 0, v125
	v_and_b32_e32 v125, 0xffff0000, v101
	s_nop 0
	v_cndmask_b32_e64 v2, v2, v100, s[42:43]
	v_cmp_lt_f32_e64 s[42:43], 0, v126
	s_nop 1
	v_cndmask_b32_e64 v2, v2, v117, s[42:43]
	v_mul_f32_e32 v100, 0x37800000, v2
	v_cndmask_b32_e32 v2, v2, v100, vcc
	v_cmp_class_f32_e32 vcc, v1, v241
	s_nop 1
	v_cndmask_b32_e32 v1, v2, v1, vcc
	v_div_scale_f32 v2, s[4:5], v1, v1, 1.0
	v_rcp_f32_e32 v100, v2
	v_div_scale_f32 v101, vcc, 1.0, v1, 1.0
	v_fma_f32 v117, -v2, v100, 1.0
	v_fmac_f32_e32 v100, v117, v100
	v_mul_f32_e32 v117, v101, v100
	v_fma_f32 v126, -v2, v117, v101
	v_fmac_f32_e32 v117, v126, v100
	v_fma_f32 v2, -v2, v117, v101
	v_div_fmas_f32 v2, v2, v100, v117
	v_div_fixup_f32 v2, v2, v1, 1.0
	v_pk_mul_f32 v[100:101], v[2:3], v[118:119] op_sel_hi:[0,1]
	v_pk_mul_f32 v[104:105], v[2:3], v[104:105] op_sel_hi:[0,1]
	v_pk_mul_f32 v[118:119], v[2:3], v[122:123] op_sel_hi:[0,1]
	v_pk_fma_f32 v[108:109], v[4:5], v[100:101], v[108:109]
	v_pk_fma_f32 v[106:107], v[6:7], v[104:105], v[106:107]
	v_pk_fma_f32 v[100:101], v[8:9], v[118:119], v[120:121]
	v_pk_mul_f32 v[104:105], v[2:3], v[124:125] op_sel_hi:[0,1]
	v_lshlrev_b32_e32 v118, 16, v96
	v_and_b32_e32 v119, 0xffff0000, v96
	v_pk_fma_f32 v[104:105], v[10:11], v[104:105], v[102:103]
	v_lshlrev_b32_e32 v102, 16, v98
	v_and_b32_e32 v103, 0xffff0000, v98
	v_pk_mul_f32 v[118:119], v[2:3], v[118:119] op_sel_hi:[0,1]
	v_lshlrev_b32_e32 v96, 16, v97
	v_and_b32_e32 v97, 0xffff0000, v97
	v_pk_fma_f32 v[102:103], v[12:13], v[118:119], v[102:103]
	v_lshlrev_b32_e32 v98, 16, v99
	v_and_b32_e32 v99, 0xffff0000, v99
	v_pk_mul_f32 v[96:97], v[2:3], v[96:97] op_sel_hi:[0,1]
	v_lshlrev_b32_e32 v118, 16, v92
	v_and_b32_e32 v119, 0xffff0000, v92
	v_pk_fma_f32 v[98:99], v[14:15], v[96:97], v[98:99]
	v_lshlrev_b32_e32 v96, 16, v94
	v_and_b32_e32 v97, 0xffff0000, v94
	v_pk_mul_f32 v[118:119], v[2:3], v[118:119] op_sel_hi:[0,1]
	v_lshlrev_b32_e32 v92, 16, v93
	v_and_b32_e32 v93, 0xffff0000, v93
	v_pk_fma_f32 v[96:97], v[16:17], v[118:119], v[96:97]
	v_lshlrev_b32_e32 v94, 16, v95
	v_and_b32_e32 v95, 0xffff0000, v95
	v_pk_mul_f32 v[92:93], v[2:3], v[92:93] op_sel_hi:[0,1]
	v_lshlrev_b32_e32 v118, 16, v88
	v_and_b32_e32 v119, 0xffff0000, v88
	v_pk_fma_f32 v[94:95], v[18:19], v[92:93], v[94:95]
	v_lshlrev_b32_e32 v92, 16, v90
	v_and_b32_e32 v93, 0xffff0000, v90
	v_pk_mul_f32 v[118:119], v[2:3], v[118:119] op_sel_hi:[0,1]
	v_lshlrev_b32_e32 v88, 16, v89
	v_and_b32_e32 v89, 0xffff0000, v89
	v_pk_fma_f32 v[92:93], v[20:21], v[118:119], v[92:93]
	v_lshlrev_b32_e32 v90, 16, v91
	v_and_b32_e32 v91, 0xffff0000, v91
	v_pk_mul_f32 v[88:89], v[2:3], v[88:89] op_sel_hi:[0,1]
	v_lshlrev_b32_e32 v118, 16, v84
	v_and_b32_e32 v119, 0xffff0000, v84
	v_pk_fma_f32 v[90:91], v[22:23], v[88:89], v[90:91]
	v_lshlrev_b32_e32 v88, 16, v86
	v_and_b32_e32 v89, 0xffff0000, v86
	v_pk_mul_f32 v[118:119], v[2:3], v[118:119] op_sel_hi:[0,1]
	v_lshlrev_b32_e32 v84, 16, v85
	v_and_b32_e32 v85, 0xffff0000, v85
	v_pk_fma_f32 v[88:89], v[24:25], v[118:119], v[88:89]
	v_lshlrev_b32_e32 v86, 16, v87
	v_and_b32_e32 v87, 0xffff0000, v87
	v_pk_mul_f32 v[84:85], v[2:3], v[84:85] op_sel_hi:[0,1]
	v_lshlrev_b32_e32 v118, 16, v80
	v_and_b32_e32 v119, 0xffff0000, v80
	v_pk_fma_f32 v[86:87], v[26:27], v[84:85], v[86:87]
	v_lshlrev_b32_e32 v84, 16, v82
	v_and_b32_e32 v85, 0xffff0000, v82
	v_pk_mul_f32 v[118:119], v[2:3], v[118:119] op_sel_hi:[0,1]
	v_lshlrev_b32_e32 v80, 16, v81
	v_and_b32_e32 v81, 0xffff0000, v81
	v_pk_fma_f32 v[84:85], v[28:29], v[118:119], v[84:85]
	v_lshlrev_b32_e32 v82, 16, v83
	v_and_b32_e32 v83, 0xffff0000, v83
	v_pk_mul_f32 v[80:81], v[2:3], v[80:81] op_sel_hi:[0,1]
	v_lshlrev_b32_e32 v118, 16, v76
	v_and_b32_e32 v119, 0xffff0000, v76
	v_lshlrev_b32_e32 v76, 16, v77
	v_and_b32_e32 v77, 0xffff0000, v77
	v_pk_fma_f32 v[82:83], v[30:31], v[80:81], v[82:83]
	v_lshlrev_b32_e32 v80, 16, v78
	v_and_b32_e32 v81, 0xffff0000, v78
	v_pk_mul_f32 v[118:119], v[2:3], v[118:119] op_sel_hi:[0,1]
	v_lshlrev_b32_e32 v78, 16, v79
	v_and_b32_e32 v79, 0xffff0000, v79
	v_pk_mul_f32 v[76:77], v[2:3], v[76:77] op_sel_hi:[0,1]
	v_pk_mul_f32 v[120:121], v[100:101], v[100:101]
	v_pk_mul_f32 v[122:123], v[104:105], v[104:105]
	v_pk_fma_f32 v[80:81], v[32:33], v[118:119], v[80:81]
	v_pk_fma_f32 v[76:77], v[34:35], v[76:77], v[78:79]
; #define GAS __attribute__((address_space(1)))
; __device__ __forceinline__ unsigned pk2(float lo, float hi) { f32x2_t_ v = {lo, hi}; bf16x2_t_ b = __builtin_convertvector(v, bf16x2_t_); return __builtin_bit_cast(unsigned, b); }
; __device__ __forceinline__ float quant_row(const f32x4 (&v)[8], unsigned char* xq, int lane) {
;     float mx = 0.f;
; #pragma unroll
;     for (int j = 0; j < 8; ++j) mx = __builtin_fmaxf(mx, __builtin_fmaxf(__builtin_fmaxf(__builtin_fabsf(v[j].x), __builtin_fabsf(v[j].y)), __builtin_fmaxf(__builtin_fabsf(v[j].z), __builtin_fabsf(v[j].w))));
;     mx = __builtin_fmaxf(wave_max(mx), 1e-20f);
; __device__ __forceinline__ void resid_rows(bf16* X, const bf16* Y, const float* PART, const float* gpost, float* RSv, float* RQv, float* fout, unsigned char* XQv, int m0, int mstep, int lane, int M_end = M) {
;     ...
;             s += (v[j].x * v[j].x + v[j].y * v[j].y) + (v[j].z * v[j].z + v[j].w * v[j].w); }
;         if (fout) { GAS f32x4* xo = (GAS f32x4*)(fout + (size_t)m * DM) + lane;
; #pragma unroll
;             for (int j = 0; j < 8; ++j) xo[64 * j] = v[j]; }
;         else { s = wave_sum(s); GAS v2u* xw = (GAS v2u*)(X + (size_t)m * DM) + lane;
; #pragma unroll
;             for (int j = 0; j < 8; ++j) { v2u w; w.x = pk2(v[j].x, v[j].y); w.y = pk2(v[j].z, v[j].w); xw[64 * j] = w; }
	v_pk_mul_f32 v[78:79], v[108:109], v[108:109]
	v_pk_mul_f32 v[118:119], v[106:107], v[106:107]
	v_add_f32_e32 v1, v123, v122
	v_add_f32_e32 v2, v120, v121
	v_add_f32_e32 v1, v2, v1
	v_add_f32_e32 v2, v119, v118
	v_add_f32_e32 v78, v78, v79
	v_pk_mul_f32 v[124:125], v[102:103], v[102:103]
	v_pk_mul_f32 v[126:127], v[98:99], v[98:99]
	v_add_f32_e32 v2, v78, v2
	v_add_f32_e32 v1, v2, v1
	v_add_f32_e32 v2, v127, v126
	v_add_f32_e32 v78, v124, v125
	v_pk_mul_f32 v[128:129], v[96:97], v[96:97]
	v_pk_mul_f32 v[130:131], v[94:95], v[94:95]
	v_add_f32_e32 v2, v78, v2
	v_add_f32_e32 v1, v2, v1
	v_add_f32_e32 v2, v131, v130
	v_add_f32_e32 v78, v128, v129
	v_pk_mul_f32 v[132:133], v[92:93], v[92:93]
	v_pk_mul_f32 v[134:135], v[90:91], v[90:91]
	v_add_f32_e32 v2, v78, v2
	v_add_f32_e32 v1, v2, v1
	v_add_f32_e32 v2, v135, v134
	v_add_f32_e32 v78, v132, v133
	v_pk_mul_f32 v[136:137], v[88:89], v[88:89]
	v_pk_mul_f32 v[138:139], v[86:87], v[86:87]
	v_add_f32_e32 v2, v78, v2
	v_add_f32_e32 v1, v2, v1
	v_add_f32_e32 v2, v139, v138
	v_add_f32_e32 v78, v136, v137
	v_pk_mul_f32 v[140:141], v[84:85], v[84:85]
	v_pk_mul_f32 v[142:143], v[82:83], v[82:83]
	v_add_f32_e32 v2, v78, v2
	v_add_f32_e32 v1, v2, v1
	v_add_f32_e32 v2, v143, v142
	v_add_f32_e32 v78, v140, v141
	v_pk_mul_f32 v[144:145], v[80:81], v[80:81]
	v_pk_mul_f32 v[146:147], v[76:77], v[76:77]
	v_add_f32_e32 v2, v78, v2
	v_add_f32_e32 v1, v2, v1
	v_add_f32_e32 v2, v147, v146
	v_add_f32_e32 v78, v144, v145
	v_add_f32_e32 v2, v78, v2
	v_add_f32_e32 v1, v2, v1
	ds_bpermute_b32 v2, v111, v1
	v_max_f32_e64 v78, |v104|, |v105|
	v_max3_f32 v78, |v100|, |v101|, v78
	v_max_f32_e64 v79, |v94|, |v95|
	v_max3_f32 v79, |v96|, |v97|, v79
	s_waitcnt lgkmcnt(0)
	v_add_f32_e32 v1, v1, v2
	ds_bpermute_b32 v2, v112, v1
	v_cvt_pk_bf16_f32 v118, v108, v109
	v_cvt_pk_bf16_f32 v119, v106, v107
	s_waitcnt lgkmcnt(0)
	v_add_f32_e32 v1, v1, v2
	ds_bpermute_b32 v2, v113, v1
	s_waitcnt lgkmcnt(0)
	v_add_f32_e32 v1, v1, v2
	ds_bpermute_b32 v2, v114, v1
	s_waitcnt lgkmcnt(0)
	v_add_f32_e32 v1, v1, v2
	ds_bpermute_b32 v2, v115, v1
	s_waitcnt lgkmcnt(0)
	v_add_f32_e32 v1, v1, v2
	v_max_f32_e64 v2, |v106|, |v107|
	v_max3_f32 v2, |v108|, |v109|, v2
	v_max3_f32 v2, v2, 0, v78
	v_max_f32_e64 v78, |v98|, |v99|
	v_max3_f32 v78, |v102|, |v103|, v78
	v_max3_f32 v2, v2, v78, v79
	v_max_f32_e64 v78, |v90|, |v91|
	v_max_f32_e64 v79, |v86|, |v87|
	v_max3_f32 v78, |v92|, |v93|, v78
	v_max3_f32 v79, |v88|, |v89|, v79
	v_max3_f32 v2, v2, v78, v79
	v_max_f32_e64 v78, |v82|, |v83|
	v_max_f32_e64 v79, |v76|, |v77|
	v_max3_f32 v78, |v84|, |v85|, v78
	v_max3_f32 v79, |v80|, |v81|, v79
	v_max3_f32 v117, v2, v78, v79
	ds_bpermute_b32 v120, v111, v117
	v_lshl_add_u64 v[78:79], s[84:85], 0, v[38:39]
	ds_bpermute_b32 v2, v116, v1
	s_waitcnt lgkmcnt(1)
	v_max_f32_e32 v120, v120, v120
	v_max_f32_e32 v117, v117, v120
	ds_bpermute_b32 v122, v112, v117
	v_add_co_u32_e32 v120, vcc, s3, v78
	v_cvt_pk_bf16_f32 v78, v100, v101
	s_nop 0
	v_addc_co_u32_e32 v121, vcc, 0, v79, vcc
	s_waitcnt vmcnt(0)
	global_store_dwordx2 v[120:121], v[118:119], off
	s_waitcnt lgkmcnt(0)
	v_max_f32_e32 v118, v122, v122
	v_max_f32_e32 v117, v117, v118
	ds_bpermute_b32 v118, v113, v117
	v_cvt_pk_bf16_f32 v79, v104, v105
	global_store_dwordx2 v[120:121], v[78:79], off offset:512
	v_cvt_pk_bf16_f32 v78, v102, v103
	v_cvt_pk_bf16_f32 v79, v98, v99
	global_store_dwordx2 v[120:121], v[78:79], off offset:1024
	s_waitcnt lgkmcnt(0)
	v_max_f32_e32 v78, v118, v118
	v_max_f32_e32 v117, v117, v78
	ds_bpermute_b32 v118, v114, v117
	v_cvt_pk_bf16_f32 v78, v96, v97
	v_cvt_pk_bf16_f32 v79, v94, v95
	global_store_dwordx2 v[120:121], v[78:79], off offset:1536
	v_cvt_pk_bf16_f32 v78, v92, v93
	s_waitcnt lgkmcnt(0)
	v_max_f32_e32 v79, v118, v118
	v_max_f32_e32 v117, v117, v79
	ds_bpermute_b32 v118, v115, v117
	v_cvt_pk_bf16_f32 v79, v90, v91
	global_store_dwordx2 v[120:121], v[78:79], off offset:2048
	v_cvt_pk_bf16_f32 v78, v88, v89
	v_cvt_pk_bf16_f32 v79, v86, v87
	s_waitcnt lgkmcnt(0)
	v_max_f32_e32 v118, v118, v118
	v_max_f32_e32 v117, v117, v118
	ds_bpermute_b32 v118, v116, v117
	global_store_dwordx2 v[120:121], v[78:79], off offset:2560
	v_cvt_pk_bf16_f32 v78, v84, v85
	v_cvt_pk_bf16_f32 v79, v82, v83
	s_mov_b32 s3, 0x1e3ce508
	global_store_dwordx2 v[120:121], v[78:79], off offset:3072
	s_waitcnt lgkmcnt(0)
; #define GAS __attribute__((address_space(1)))
; __device__ __forceinline__ float quant_row(const f32x4 (&v)[8], unsigned char* xq, int lane) {
;     float mx = 0.f;
; #pragma unroll
;     for (int j = 0; j < 8; ++j) mx = __builtin_fmaxf(mx, __builtin_fmaxf(__builtin_fmaxf(__builtin_fabsf(v[j].x), __builtin_fabsf(v[j].y)), __builtin_fmaxf(__builtin_fabsf(v[j].z), __builtin_fabsf(v[j].w))));
;     mx = __builtin_fmaxf(wave_max(mx), 1e-20f);
;     const float q = 127.0f / mx;
;     GAS unsigned* o4 = (GAS unsigned*)xq + lane;
; #pragma unroll
;     for (int j = 0; j < 8; ++j) o4[64 * j] = q4(v[j], q);
;     return mx * (1.0f / 127.0f);
; __device__ __forceinline__ void resid_rows(bf16* X, const bf16* Y, const float* PART, const float* gpost, float* RSv, float* RQv, float* fout, unsigned char* XQv, int m0, int mstep, int lane, int M_end = M) {
;     ...
;             const float dq = quant_row(v, XQv + (size_t)m * DM, lane);
;             if (lane == 0) { const float r = 1.f / sqrtf(s * (1.f / DM) + NORM_EPS); RSv[m] = r; RQv[m] = r * dq; } }
	v_max3_f32 v78, v117, v118, s3
	s_mov_b32 s3, 0x42fe0000
	v_div_scale_f32 v79, s[4:5], v78, v78, s3
	v_rcp_f32_e32 v117, v79
	v_cvt_pk_bf16_f32 v118, v80, v81
	v_cvt_pk_bf16_f32 v119, v76, v77
	global_store_dwordx2 v[120:121], v[118:119], off offset:3584
	v_fma_f32 v118, -v79, v117, 1.0
	v_fmac_f32_e32 v117, v118, v117
	v_div_scale_f32 v118, vcc, s3, v78, s3
	v_mul_f32_e32 v119, v118, v117
	v_fma_f32 v120, -v79, v119, v118
	v_fmac_f32_e32 v119, v120, v117
	v_fma_f32 v79, -v79, v119, v118
	v_div_fmas_f32 v79, v79, v117, v119
	v_div_fixup_f32 v79, v79, v78, s3
	v_mul_f32_e32 v109, v109, v79
	v_mul_f32_e32 v108, v108, v79
	v_rndne_f32_e32 v109, v109
	v_mul_f32_e32 v106, v106, v79
	v_mul_f32_e32 v107, v107, v79
	v_mul_f32_e32 v101, v101, v79
	v_rndne_f32_e32 v108, v108
	v_cvt_i32_f32_e32 v109, v109
	v_rndne_f32_e32 v106, v106
	v_rndne_f32_e32 v107, v107
	v_mul_f32_e32 v100, v100, v79
	v_rndne_f32_e32 v101, v101
	v_mul_f32_e32 v104, v104, v79
	v_mul_f32_e32 v105, v105, v79
	v_cvt_i32_f32_e32 v108, v108
	v_cvt_i32_f32_sdwa v106, v106 dst_sel:WORD_1 dst_unused:UNUSED_PAD src0_sel:DWORD
	v_cvt_i32_f32_e32 v107, v107
	v_rndne_f32_e32 v100, v100
	v_cvt_i32_f32_e32 v101, v101
	v_rndne_f32_e32 v104, v104
	v_rndne_f32_e32 v105, v105
	v_cvt_i32_f32_e32 v100, v100
	v_cvt_i32_f32_sdwa v104, v104 dst_sel:WORD_1 dst_unused:UNUSED_PAD src0_sel:DWORD
	v_cvt_i32_f32_e32 v105, v105
	v_lshlrev_b32_e32 v109, 8, v109
	v_lshl_add_u64 v[118:119], s[84:85], 0, v[36:37]
	v_and_b32_e32 v109, 0xff00, v109
	v_and_b32_e32 v106, 0xff0000, v106
	v_perm_b32 v107, v107, v108, s17
	s_mov_b32 s3, 0x8800000
	v_lshlrev_b32_e32 v101, 8, v101
	v_or3_b32 v108, v107, v109, v106
	v_add_co_u32_e32 v106, vcc, s3, v118
	v_and_b32_e32 v101, 0xff00, v101
	v_and_b32_e32 v104, 0xff0000, v104
	v_perm_b32 v100, v105, v100, s17
	v_addc_co_u32_e32 v107, vcc, 0, v119, vcc
	v_or3_b32 v100, v100, v101, v104
	v_mul_f32_e32 v101, v103, v79
	v_mul_f32_e32 v97, v97, v79
	v_mul_f32_e32 v93, v93, v79
	v_mul_f32_e32 v89, v89, v79
	v_mul_f32_e32 v85, v85, v79
	v_mul_f32_e32 v81, v81, v79
	global_store_dword v[106:107], v100, off offset:256
	v_mul_f32_e32 v100, v102, v79
	v_rndne_f32_e32 v101, v101
	v_mul_f32_e32 v98, v98, v79
	v_mul_f32_e32 v99, v99, v79
	v_mul_f32_e32 v96, v96, v79
	v_rndne_f32_e32 v97, v97
	v_mul_f32_e32 v94, v94, v79
	v_mul_f32_e32 v95, v95, v79
	v_mul_f32_e32 v92, v92, v79
	v_rndne_f32_e32 v93, v93
	v_mul_f32_e32 v90, v90, v79
	v_mul_f32_e32 v91, v91, v79
	v_mul_f32_e32 v88, v88, v79
	v_rndne_f32_e32 v89, v89
	v_mul_f32_e32 v86, v86, v79
	v_mul_f32_e32 v87, v87, v79
	v_mul_f32_e32 v84, v84, v79
	v_rndne_f32_e32 v85, v85
	v_mul_f32_e32 v82, v82, v79
	v_mul_f32_e32 v83, v83, v79
	v_mul_f32_e32 v80, v80, v79
	v_rndne_f32_e32 v81, v81
	v_mul_f32_e32 v76, v76, v79
	v_mul_f32_e32 v77, v77, v79
	v_rndne_f32_e32 v100, v100
	v_cvt_i32_f32_e32 v101, v101
	v_rndne_f32_e32 v98, v98
	v_rndne_f32_e32 v99, v99
	v_rndne_f32_e32 v96, v96
	v_cvt_i32_f32_e32 v97, v97
	v_rndne_f32_e32 v94, v94
	v_rndne_f32_e32 v95, v95
	v_rndne_f32_e32 v92, v92
	v_cvt_i32_f32_e32 v93, v93
	v_rndne_f32_e32 v90, v90
	v_rndne_f32_e32 v91, v91
	v_rndne_f32_e32 v88, v88
	v_cvt_i32_f32_e32 v89, v89
	v_rndne_f32_e32 v86, v86
	v_rndne_f32_e32 v87, v87
	v_rndne_f32_e32 v84, v84
	v_cvt_i32_f32_e32 v85, v85
	v_rndne_f32_e32 v82, v82
	v_rndne_f32_e32 v83, v83
	v_rndne_f32_e32 v80, v80
	v_cvt_i32_f32_e32 v81, v81
	v_rndne_f32_e32 v76, v76
	v_rndne_f32_e32 v77, v77
	v_cvt_i32_f32_e32 v100, v100
	v_cvt_i32_f32_sdwa v98, v98 dst_sel:WORD_1 dst_unused:UNUSED_PAD src0_sel:DWORD
	v_cvt_i32_f32_e32 v99, v99
	v_cvt_i32_f32_e32 v96, v96
	v_cvt_i32_f32_sdwa v94, v94 dst_sel:WORD_1 dst_unused:UNUSED_PAD src0_sel:DWORD
	v_cvt_i32_f32_e32 v95, v95
	v_cvt_i32_f32_e32 v92, v92
	v_cvt_i32_f32_sdwa v90, v90 dst_sel:WORD_1 dst_unused:UNUSED_PAD src0_sel:DWORD
	v_cvt_i32_f32_e32 v91, v91
	v_cvt_i32_f32_e32 v88, v88
	v_cvt_i32_f32_sdwa v86, v86 dst_sel:WORD_1 dst_unused:UNUSED_PAD src0_sel:DWORD
	v_cvt_i32_f32_e32 v87, v87
	v_cvt_i32_f32_e32 v84, v84
	v_cvt_i32_f32_sdwa v82, v82 dst_sel:WORD_1 dst_unused:UNUSED_PAD src0_sel:DWORD
	v_cvt_i32_f32_e32 v83, v83
	v_cvt_i32_f32_e32 v80, v80
	v_cvt_i32_f32_sdwa v76, v76 dst_sel:WORD_1 dst_unused:UNUSED_PAD src0_sel:DWORD
	v_cvt_i32_f32_e32 v77, v77
	v_lshlrev_b32_e32 v101, 8, v101
	v_lshlrev_b32_e32 v97, 8, v97
	v_lshlrev_b32_e32 v93, 8, v93
	v_lshlrev_b32_e32 v89, 8, v89
	v_lshlrev_b32_e32 v85, 8, v85
	v_lshlrev_b32_e32 v79, 8, v81
	v_and_b32_e32 v101, 0xff00, v101
	v_and_b32_e32 v98, 0xff0000, v98
	v_perm_b32 v99, v99, v100, s17
	v_and_b32_e32 v97, 0xff00, v97
	v_and_b32_e32 v94, 0xff0000, v94
	v_perm_b32 v95, v95, v96, s17
	v_and_b32_e32 v93, 0xff00, v93
	v_and_b32_e32 v90, 0xff0000, v90
	v_perm_b32 v91, v91, v92, s17
	v_and_b32_e32 v89, 0xff00, v89
	v_and_b32_e32 v86, 0xff0000, v86
	v_perm_b32 v87, v87, v88, s17
	v_and_b32_e32 v85, 0xff00, v85
	v_and_b32_e32 v82, 0xff0000, v82
	v_perm_b32 v83, v83, v84, s17
	v_and_b32_e32 v79, 0xff00, v79
	v_and_b32_e32 v76, 0xff0000, v76
	v_perm_b32 v77, v77, v80, s17
	v_or3_b32 v98, v99, v101, v98
	v_or3_b32 v94, v95, v97, v94
	v_or3_b32 v90, v91, v93, v90
	v_or3_b32 v86, v87, v89, v86
	v_or3_b32 v82, v83, v85, v82
	v_or3_b32 v76, v77, v79, v76
	global_store_dword v[106:107], v108, off
	global_store_dword v[106:107], v98, off offset:512
	global_store_dword v[106:107], v94, off offset:768
	global_store_dword v[106:107], v90, off offset:1024
	global_store_dword v[106:107], v86, off offset:1280
	global_store_dword v[106:107], v82, off offset:1536
	global_store_dword v[106:107], v76, off offset:1792
	s_and_saveexec_b64 s[48:49], s[40:41]
	s_cbranch_execz .LBB0_1022
	v_add_f32_e32 v1, v1, v2
	v_fmamk_f32 v1, v1, 0x3a000000, v240
	v_mul_f32_e32 v2, 0x4f800000, v1
	v_cmp_gt_f32_e32 vcc, s82, v1
	s_nop 1
	v_cndmask_b32_e32 v1, v1, v2, vcc
	v_sqrt_f32_e32 v2, v1
	s_nop 0
	v_add_u32_e32 v76, -1, v2
	v_fma_f32 v79, -v76, v2, v1
	v_add_u32_e32 v77, 1, v2
	v_cmp_ge_f32_e64 s[42:43], 0, v79
	s_nop 1
	v_cndmask_b32_e64 v76, v2, v76, s[42:43]
	v_fma_f32 v2, -v77, v2, v1
	v_cmp_lt_f32_e64 s[42:43], 0, v2
	s_nop 1
	v_cndmask_b32_e64 v2, v76, v77, s[42:43]
	v_mul_f32_e32 v76, 0x37800000, v2
	v_cndmask_b32_e32 v2, v2, v76, vcc
	v_cmp_class_f32_e32 vcc, v1, v241
	v_mul_f32_e32 v77, 0x3c010204, v78
	s_nop 0
	v_cndmask_b32_e32 v1, v2, v1, vcc
	v_div_scale_f32 v2, s[4:5], v1, v1, 1.0
	v_rcp_f32_e32 v76, v2
	s_add_u32 s4, s84, s44
	s_addc_u32 s5, s85, s45
	v_fma_f32 v78, -v2, v76, 1.0
	v_fmac_f32_e32 v76, v78, v76
	v_div_scale_f32 v78, vcc, 1.0, v1, 1.0
	v_mul_f32_e32 v79, v78, v76
	v_fma_f32 v80, -v2, v79, v78
	v_fmac_f32_e32 v79, v80, v76
	v_fma_f32 v2, -v2, v79, v78
	v_div_fmas_f32 v2, v2, v76, v79
	v_div_fixup_f32 v1, v2, v1, 1.0
	global_store_dword v236, v1, s[4:5]
	v_mul_f32_e32 v1, v77, v1
	global_store_dword v237, v1, s[4:5]
	s_branch .LBB0_1022

; #define GAS __attribute__((address_space(1)))
; __device__ __forceinline__ void resid_rows(bf16* X, const bf16* Y, const float* PART, const float* gpost, float* RSv, float* RQv, float* fout, unsigned char* XQv, int m0, int mstep, int lane, int M_end = M) {
;     ...
;     while (m < M) {
;         const int mn = m + mstep;
;         if (mn < M) { const GAS v2u* xr = (const GAS v2u*)(X + (size_t)mn * DM) + lane; const GAS v2u* yr = (const GAS v2u*)(Y + (size_t)mn * DM) + lane; np = (lane < 32) ? PART[(size_t)mn * 32 + lane] : 0.f;
; #pragma unroll
;             for (int j = 0; j < 8; ++j) { nx[j] = xr[64 * j]; ny[j] = yr[64 * j]; } }
;     ...
; #pragma unroll
;         for (int j = 0; j < 8; ++j) { cx[j] = nx[j]; cy[j] = ny[j]; }
;         cp = np; m = mn; }
.LBB0_1346:
	v_readlane_b32 s18, v254, 41
	v_readlane_b32 s19, v254, 42
	v_readlane_b32 s40, v255, 10
	s_add_u32 s46, s46, s24
	v_lshl_add_u64 v[70:71], v[70:71], 0, s[18:19]
	v_lshl_add_u64 v[74:75], v[74:75], 0, s[18:19]
	v_readlane_b32 s18, v254, 47
	v_readlane_b32 s41, v255, 11
	v_readlane_b32 s19, v254, 48
	s_addc_u32 s47, s47, s25
	v_lshl_add_u64 v[68:69], v[68:69], 0, s[50:51]
	v_lshl_add_u64 v[72:73], v[72:73], 0, s[40:41]
	v_lshl_add_u64 v[76:77], v[76:77], 0, s[18:19]
	s_andn2_b64 vcc, exec, s[48:49]
	s_waitcnt lgkmcnt(0)
	v_mov_b64_e32 v[110:111], v[92:93]
	v_mov_b64_e32 v[64:65], v[90:91]
	v_mov_b64_e32 v[60:61], v[88:89]
	v_mov_b64_e32 v[56:57], v[86:87]
	v_mov_b64_e32 v[52:53], v[84:85]
	v_mov_b64_e32 v[48:49], v[82:83]
	v_mov_b64_e32 v[44:45], v[80:81]
	v_mov_b64_e32 v[40:41], v[78:79]
	v_mov_b64_e32 v[66:67], v[102:103]
	v_mov_b64_e32 v[62:63], v[104:105]
	v_mov_b64_e32 v[58:59], v[106:107]
	v_mov_b64_e32 v[54:55], v[108:109]
	v_mov_b64_e32 v[50:51], v[94:95]
	v_mov_b64_e32 v[46:47], v[96:97]
	v_mov_b64_e32 v[42:43], v[98:99]
	v_mov_b64_e32 v[38:39], v[100:101]
	v_mov_b32_e32 v36, v113
	s_cbranch_vccz .LBB0_1356
	s_add_i32 s4, s4, s94
	s_cmpk_gt_i32 s4, 0x3fff
	s_cselect_b64 s[48:49], -1, 0
	s_and_b64 vcc, exec, s[48:49]
	s_cbranch_vccnz .LBB0_1351
	v_mov_b32_e32 v113, 0
	s_and_saveexec_b64 s[40:41], s[36:37]
	s_cbranch_execz .Lresw2_1350
	v_lshl_add_u64 v[78:79], s[84:85], 0, v[76:77]
	global_load_dword v113, v[78:79], off
.Lresw2_1350:
	s_or_b64 exec, exec, s[40:41]
	v_lshl_add_u64 v[78:79], s[84:85], 0, v[74:75]
	v_add_co_u32_e32 v92, vcc, 0x23800000, v78
	s_nop 1
	v_addc_co_u32_e32 v93, vcc, 0, v79, vcc
	v_add_co_u32_e32 v102, vcc, 0x2b800000, v78
	s_nop 1
	v_addc_co_u32_e32 v103, vcc, 0, v79, vcc
	global_load_dwordx2 v[78:79], v[92:93], off
	global_load_dwordx2 v[80:81], v[92:93], off offset:512
	global_load_dwordx2 v[82:83], v[92:93], off offset:1024
	global_load_dwordx2 v[84:85], v[92:93], off offset:1536
	global_load_dwordx2 v[100:101], v[102:103], off
	global_load_dwordx2 v[98:99], v[102:103], off offset:512
	global_load_dwordx2 v[96:97], v[102:103], off offset:1024
	global_load_dwordx2 v[94:95], v[102:103], off offset:1536
	global_load_dwordx2 v[86:87], v[92:93], off offset:2048
	global_load_dwordx2 v[88:89], v[92:93], off offset:2560
	global_load_dwordx2 v[90:91], v[92:93], off offset:3072
	s_nop 0
	global_load_dwordx2 v[92:93], v[92:93], off offset:3584
	s_nop 0
	global_load_dwordx2 v[108:109], v[102:103], off offset:2048
	global_load_dwordx2 v[106:107], v[102:103], off offset:2560
	global_load_dwordx2 v[104:105], v[102:103], off offset:3072
	s_nop 0
	global_load_dwordx2 v[102:103], v[102:103], off offset:3584
	s_branch .LBB0_1351

; #define GAS __attribute__((address_space(1)))
; __device__ __forceinline__ void resid_rows(bf16* X, const bf16* Y, const float* PART, const float* gpost, float* RSv, float* RQv, float* fout, unsigned char* XQv, int m0, int mstep, int lane, int M_end = M) {
;     ...
;         const float ps = wave_sum(cp); const float rs1 = 1.f / sqrtf(ps * (1.f / DM) + NORM_EPS);
;         f32x4 v[8]; float s = 0.f;
; #pragma unroll
;         for (int j = 0; j < 8; ++j) { const v2u x = cx[j], y = cy[j];
;             v[j].x = bflo(x.x) + bflo(y.x) * rs1 * g[j].x; v[j].y = bfhi(x.x) + bfhi(y.x) * rs1 * g[j].y; v[j].z = bflo(x.y) + bflo(y.y) * rs1 * g[j].z; v[j].w = bfhi(x.y) + bfhi(y.y) * rs1 * g[j].w;
;             s += (v[j].x * v[j].x + v[j].y * v[j].y) + (v[j].z * v[j].z + v[j].w * v[j].w); }
;         if (fout) { GAS f32x4* xo = (GAS f32x4*)(fout + (size_t)m * DM) + lane;
; #pragma unroll
;             for (int j = 0; j < 8; ++j) xo[64 * j] = v[j]; }
.LBB0_1351:
	ds_bpermute_b32 v37, v114, v36
	s_waitcnt lgkmcnt(0)
	v_add_f32_e32 v36, v36, v37
	ds_bpermute_b32 v37, v115, v36
	s_waitcnt lgkmcnt(0)
	v_add_f32_e32 v36, v36, v37
	ds_bpermute_b32 v37, v116, v36
	s_waitcnt lgkmcnt(0)
	v_add_f32_e32 v36, v36, v37
	ds_bpermute_b32 v37, v117, v36
	s_waitcnt lgkmcnt(0)
	v_add_f32_e32 v36, v36, v37
	ds_bpermute_b32 v37, v118, v36
	s_waitcnt lgkmcnt(0)
	v_add_f32_e32 v36, v36, v37
	ds_bpermute_b32 v37, v119, v36
	s_waitcnt lgkmcnt(0)
	v_add_f32_e32 v36, v36, v37
	v_fmamk_f32 v36, v36, 0x3a000000, v240
	v_cmp_gt_f32_e32 vcc, s82, v36
	v_mul_f32_e32 v37, 0x4f800000, v36
	s_nop 0
	v_cndmask_b32_e32 v36, v36, v37, vcc
	v_sqrt_f32_e32 v37, v36
	s_nop 0
	v_add_u32_e32 v112, -1, v37
	v_fma_f32 v120, -v112, v37, v36
	v_cmp_ge_f32_e64 s[40:41], 0, v120
	v_add_u32_e32 v120, 1, v37
	s_nop 0
	v_cndmask_b32_e64 v112, v37, v112, s[40:41]
	v_fma_f32 v37, -v120, v37, v36
	v_cmp_lt_f32_e64 s[40:41], 0, v37
	s_nop 1
	v_cndmask_b32_e64 v37, v112, v120, s[40:41]
	v_mul_f32_e32 v112, 0x37800000, v37
	v_cndmask_b32_e32 v37, v37, v112, vcc
	v_cmp_class_f32_e32 vcc, v36, v241
	s_nop 1
	v_cndmask_b32_e32 v36, v37, v36, vcc
	v_div_scale_f32 v37, s[18:19], v36, v36, 1.0
	v_rcp_f32_e32 v112, v37
	s_nop 0
	v_fma_f32 v120, -v37, v112, 1.0
	v_fmac_f32_e32 v112, v120, v112
	v_div_scale_f32 v120, vcc, 1.0, v36, 1.0
	v_mul_f32_e32 v121, v120, v112
	v_fma_f32 v122, -v37, v121, v120
	v_fmac_f32_e32 v121, v122, v112
	v_fma_f32 v37, -v37, v121, v120
	v_div_fmas_f32 v37, v37, v112, v121
	v_div_fixup_f32 v112, v37, v36, 1.0
	v_lshlrev_b32_e32 v120, 16, v38
	v_and_b32_e32 v121, 0xffff0000, v38
	v_lshlrev_b32_e32 v36, 16, v40
	v_and_b32_e32 v37, 0xffff0000, v40
	v_pk_mul_f32 v[120:121], v[112:113], v[120:121] op_sel_hi:[0,1]
	v_lshlrev_b32_e32 v38, 16, v39
	v_and_b32_e32 v39, 0xffff0000, v39
	v_pk_fma_f32 v[36:37], v[4:5], v[120:121], v[36:37]
	v_lshlrev_b32_e32 v40, 16, v41
	v_and_b32_e32 v41, 0xffff0000, v41
	v_pk_mul_f32 v[38:39], v[112:113], v[38:39] op_sel_hi:[0,1]
	v_lshlrev_b32_e32 v120, 16, v42
	v_and_b32_e32 v121, 0xffff0000, v42
	v_pk_fma_f32 v[38:39], v[6:7], v[38:39], v[40:41]
	v_lshlrev_b32_e32 v40, 16, v44
	v_and_b32_e32 v41, 0xffff0000, v44
	v_pk_mul_f32 v[120:121], v[112:113], v[120:121] op_sel_hi:[0,1]
	v_lshlrev_b32_e32 v42, 16, v43
	v_and_b32_e32 v43, 0xffff0000, v43
	v_pk_fma_f32 v[40:41], v[8:9], v[120:121], v[40:41]
	v_lshlrev_b32_e32 v44, 16, v45
	v_and_b32_e32 v45, 0xffff0000, v45
	v_pk_mul_f32 v[42:43], v[112:113], v[42:43] op_sel_hi:[0,1]
	v_lshlrev_b32_e32 v120, 16, v46
	v_and_b32_e32 v121, 0xffff0000, v46
	v_pk_fma_f32 v[42:43], v[10:11], v[42:43], v[44:45]
	v_lshlrev_b32_e32 v44, 16, v48
	v_and_b32_e32 v45, 0xffff0000, v48
	v_pk_mul_f32 v[120:121], v[112:113], v[120:121] op_sel_hi:[0,1]
	v_lshlrev_b32_e32 v46, 16, v47
	v_and_b32_e32 v47, 0xffff0000, v47
	v_pk_fma_f32 v[44:45], v[12:13], v[120:121], v[44:45]
	v_lshlrev_b32_e32 v48, 16, v49
	v_and_b32_e32 v49, 0xffff0000, v49
	v_pk_mul_f32 v[46:47], v[112:113], v[46:47] op_sel_hi:[0,1]
	v_lshlrev_b32_e32 v120, 16, v50
	v_and_b32_e32 v121, 0xffff0000, v50
	v_pk_fma_f32 v[46:47], v[14:15], v[46:47], v[48:49]
	v_lshlrev_b32_e32 v48, 16, v52
	v_and_b32_e32 v49, 0xffff0000, v52
	v_pk_mul_f32 v[120:121], v[112:113], v[120:121] op_sel_hi:[0,1]
	v_lshlrev_b32_e32 v50, 16, v51
	v_and_b32_e32 v51, 0xffff0000, v51
	v_pk_fma_f32 v[48:49], v[16:17], v[120:121], v[48:49]
	v_lshlrev_b32_e32 v52, 16, v53
	v_and_b32_e32 v53, 0xffff0000, v53
	v_pk_mul_f32 v[50:51], v[112:113], v[50:51] op_sel_hi:[0,1]
	v_lshlrev_b32_e32 v120, 16, v54
	v_and_b32_e32 v121, 0xffff0000, v54
	v_pk_fma_f32 v[50:51], v[18:19], v[50:51], v[52:53]
	v_lshlrev_b32_e32 v52, 16, v56
	v_and_b32_e32 v53, 0xffff0000, v56
	v_pk_mul_f32 v[120:121], v[112:113], v[120:121] op_sel_hi:[0,1]
	v_lshlrev_b32_e32 v54, 16, v55
	v_and_b32_e32 v55, 0xffff0000, v55
	v_pk_fma_f32 v[52:53], v[20:21], v[120:121], v[52:53]
	v_lshlrev_b32_e32 v56, 16, v57
	v_and_b32_e32 v57, 0xffff0000, v57
	v_pk_mul_f32 v[54:55], v[112:113], v[54:55] op_sel_hi:[0,1]
	v_lshlrev_b32_e32 v120, 16, v58
	v_and_b32_e32 v121, 0xffff0000, v58
	v_pk_fma_f32 v[54:55], v[22:23], v[54:55], v[56:57]
	v_lshlrev_b32_e32 v56, 16, v60
	v_and_b32_e32 v57, 0xffff0000, v60
	v_pk_mul_f32 v[120:121], v[112:113], v[120:121] op_sel_hi:[0,1]
	v_lshlrev_b32_e32 v58, 16, v59
	v_and_b32_e32 v59, 0xffff0000, v59
	v_pk_fma_f32 v[56:57], v[24:25], v[120:121], v[56:57]
	v_lshlrev_b32_e32 v60, 16, v61
	v_and_b32_e32 v61, 0xffff0000, v61
	v_pk_mul_f32 v[58:59], v[112:113], v[58:59] op_sel_hi:[0,1]
	v_lshlrev_b32_e32 v120, 16, v62
	v_and_b32_e32 v121, 0xffff0000, v62
	v_pk_fma_f32 v[58:59], v[26:27], v[58:59], v[60:61]
	v_lshlrev_b32_e32 v60, 16, v64
	v_and_b32_e32 v61, 0xffff0000, v64
	v_pk_mul_f32 v[120:121], v[112:113], v[120:121] op_sel_hi:[0,1]
	v_lshlrev_b32_e32 v62, 16, v63
	v_and_b32_e32 v63, 0xffff0000, v63
	v_pk_fma_f32 v[60:61], v[28:29], v[120:121], v[60:61]
	v_lshlrev_b32_e32 v64, 16, v65
	v_and_b32_e32 v65, 0xffff0000, v65
	v_pk_mul_f32 v[62:63], v[112:113], v[62:63] op_sel_hi:[0,1]
	v_lshlrev_b32_e32 v120, 16, v66
	v_and_b32_e32 v121, 0xffff0000, v66
	v_lshlrev_b32_e32 v66, 16, v67
	v_and_b32_e32 v67, 0xffff0000, v67
	v_pk_fma_f32 v[62:63], v[30:31], v[62:63], v[64:65]
	v_lshlrev_b32_e32 v64, 16, v110
	v_and_b32_e32 v65, 0xffff0000, v110
	v_pk_mul_f32 v[120:121], v[112:113], v[120:121] op_sel_hi:[0,1]
	v_lshlrev_b32_e32 v110, 16, v111
	v_and_b32_e32 v111, 0xffff0000, v111
	v_pk_mul_f32 v[66:67], v[112:113], v[66:67] op_sel_hi:[0,1]
	v_pk_fma_f32 v[64:65], v[32:33], v[120:121], v[64:65]
	v_pk_fma_f32 v[66:67], v[34:35], v[66:67], v[110:111]
	s_waitcnt vmcnt(0)
	s_andn2_b64 vcc, exec, s[44:45]
	s_cbranch_vccnz .LBB0_1353
	global_store_dwordx4 v[72:73], v[36:39], off offset:-4096
	global_store_dwordx4 v[72:73], v[40:43], off offset:-3072
	global_store_dwordx4 v[72:73], v[44:47], off offset:-2048
	global_store_dwordx4 v[72:73], v[48:51], off offset:-1024
	global_store_dwordx4 v[72:73], v[52:55], off
	global_store_dwordx4 v[72:73], v[56:59], off offset:1024
	global_store_dwordx4 v[72:73], v[60:63], off offset:2048
	global_store_dwordx4 v[72:73], v[64:67], off offset:3072
	s_cbranch_execnz .LBB0_1346
	s_branch .LBB0_1354

; #define GAS __attribute__((address_space(1)))
; __device__ __forceinline__ void resid_rows(bf16* X, const bf16* Y, const float* PART, const float* gpost, float* RSv, float* RQv, float* fout, unsigned char* XQv, int m0, int mstep, int lane, int M_end = M) {
;     ...
;     while (m < M) {
;         const int mn = m + mstep;
;         if (mn < M) { const GAS v2u* xr = (const GAS v2u*)(X + (size_t)mn * DM) + lane; const GAS v2u* yr = (const GAS v2u*)(Y + (size_t)mn * DM) + lane; np = (lane < 32) ? PART[(size_t)mn * 32 + lane] : 0.f;
; #pragma unroll
;             for (int j = 0; j < 8; ++j) { nx[j] = xr[64 * j]; ny[j] = yr[64 * j]; } }
;     ...
; #pragma unroll
;         for (int j = 0; j < 8; ++j) { cx[j] = nx[j]; cy[j] = ny[j]; }
;         cp = np; m = mn; }
.LBB0_1363:
	s_mov_b64 s[18:19], 0x80000
	v_lshl_add_u64 v[68:69], v[68:69], 0, s[18:19]
	s_mov_b64 s[18:19], 0x100000
	s_add_u32 s42, s42, 0x400
	v_lshl_add_u64 v[70:71], v[70:71], 0, s[18:19]
	s_mov_b64 s[24:25], 0x200000
	v_lshl_add_u64 v[74:75], v[74:75], 0, s[18:19]
	s_mov_b64 s[18:19], 0x8000
	s_addc_u32 s43, s43, 0
	v_lshl_add_u64 v[72:73], v[72:73], 0, s[24:25]
	v_lshl_add_u64 v[76:77], v[76:77], 0, s[18:19]
	s_and_b64 vcc, exec, s[46:47]
	v_mov_b64_e32 v[110:111], v[92:93]
	v_mov_b64_e32 v[64:65], v[90:91]
	v_mov_b64_e32 v[60:61], v[88:89]
	v_mov_b64_e32 v[56:57], v[86:87]
	v_mov_b64_e32 v[52:53], v[84:85]
	v_mov_b64_e32 v[48:49], v[82:83]
	v_mov_b64_e32 v[44:45], v[80:81]
	v_mov_b64_e32 v[40:41], v[78:79]
	v_mov_b64_e32 v[66:67], v[102:103]
	v_mov_b64_e32 v[62:63], v[104:105]
	v_mov_b64_e32 v[58:59], v[106:107]
	v_mov_b64_e32 v[54:55], v[108:109]
	v_mov_b64_e32 v[50:51], v[94:95]
	v_mov_b64_e32 v[46:47], v[96:97]
	v_mov_b64_e32 v[42:43], v[98:99]
	v_mov_b64_e32 v[38:39], v[100:101]
	v_mov_b32_e32 v119, v112
	s_cbranch_vccnz .LBB0_1373
	s_addk_i32 s4, 0x100
	v_readlane_b32 s0, v253, 35
	s_cmp_ge_i32 s4, s0
	s_cselect_b64 s[46:47], -1, 0
	s_and_b64 vcc, exec, s[46:47]
	s_cbranch_vccnz .LBB0_1368
	v_mov_b32_e32 v112, 0
	s_and_saveexec_b64 s[40:41], s[36:37]
	s_cbranch_execz .Lresw3_1367
	v_lshl_add_u64 v[36:37], s[84:85], 0, v[76:77]
	global_load_dword v112, v[36:37], off
.Lresw3_1367:
	s_or_b64 exec, exec, s[40:41]
	v_lshl_add_u64 v[36:37], s[84:85], 0, v[74:75]
	v_add_co_u32_e32 v92, vcc, 0x23800000, v36
	s_nop 1
	v_addc_co_u32_e32 v93, vcc, 0, v37, vcc
	v_add_co_u32_e32 v36, vcc, 0x2b800000, v36
	s_nop 1
	v_addc_co_u32_e32 v37, vcc, 0, v37, vcc
	global_load_dwordx2 v[78:79], v[92:93], off
	global_load_dwordx2 v[80:81], v[92:93], off offset:512
	global_load_dwordx2 v[82:83], v[92:93], off offset:1024
	global_load_dwordx2 v[84:85], v[92:93], off offset:1536
	global_load_dwordx2 v[100:101], v[36:37], off
	global_load_dwordx2 v[98:99], v[36:37], off offset:512
	global_load_dwordx2 v[96:97], v[36:37], off offset:1024
	global_load_dwordx2 v[94:95], v[36:37], off offset:1536
	global_load_dwordx2 v[86:87], v[92:93], off offset:2048
	global_load_dwordx2 v[88:89], v[92:93], off offset:2560
	global_load_dwordx2 v[90:91], v[92:93], off offset:3072
	s_nop 0
	global_load_dwordx2 v[92:93], v[92:93], off offset:3584
	s_nop 0
	global_load_dwordx2 v[108:109], v[36:37], off offset:2048
	global_load_dwordx2 v[106:107], v[36:37], off offset:2560
	global_load_dwordx2 v[104:105], v[36:37], off offset:3072
	global_load_dwordx2 v[102:103], v[36:37], off offset:3584
	s_branch .LBB0_1368

; #define GAS __attribute__((address_space(1)))
; __device__ __forceinline__ void resid_rows(bf16* X, const bf16* Y, const float* PART, const float* gpost, float* RSv, float* RQv, float* fout, unsigned char* XQv, int m0, int mstep, int lane, int M_end = M) {
;     ...
;         const float ps = wave_sum(cp); const float rs1 = 1.f / sqrtf(ps * (1.f / DM) + NORM_EPS);
;         f32x4 v[8]; float s = 0.f;
; #pragma unroll
;         for (int j = 0; j < 8; ++j) { const v2u x = cx[j], y = cy[j];
;             v[j].x = bflo(x.x) + bflo(y.x) * rs1 * g[j].x; v[j].y = bfhi(x.x) + bfhi(y.x) * rs1 * g[j].y; v[j].z = bflo(x.y) + bflo(y.y) * rs1 * g[j].z; v[j].w = bfhi(x.y) + bfhi(y.y) * rs1 * g[j].w;
;             s += (v[j].x * v[j].x + v[j].y * v[j].y) + (v[j].z * v[j].z + v[j].w * v[j].w); }
;         if (fout) { GAS f32x4* xo = (GAS f32x4*)(fout + (size_t)m * DM) + lane;
; #pragma unroll
;             for (int j = 0; j < 8; ++j) xo[64 * j] = v[j]; }
.LBB0_1368:
	ds_bpermute_b32 v1, v113, v119
	v_and_b32_e32 v121, 0xffff0000, v38
	s_waitcnt lgkmcnt(0)
	v_add_f32_e32 v1, v119, v1
	ds_bpermute_b32 v2, v114, v1
	s_waitcnt lgkmcnt(0)
	v_add_f32_e32 v1, v1, v2
	ds_bpermute_b32 v2, v115, v1
	s_waitcnt lgkmcnt(0)
	v_add_f32_e32 v1, v1, v2
	ds_bpermute_b32 v2, v116, v1
	s_waitcnt lgkmcnt(0)
	v_add_f32_e32 v1, v1, v2
	ds_bpermute_b32 v2, v117, v1
	s_waitcnt lgkmcnt(0)
	v_add_f32_e32 v1, v1, v2
	ds_bpermute_b32 v2, v118, v1
	s_waitcnt lgkmcnt(0)
	v_add_f32_e32 v1, v1, v2
	v_fmamk_f32 v1, v1, 0x3a000000, v240
	v_cmp_gt_f32_e32 vcc, s82, v1
	v_mul_f32_e32 v2, 0x4f800000, v1
	s_nop 0
	v_cndmask_b32_e32 v1, v1, v2, vcc
	v_sqrt_f32_e32 v2, v1
	s_nop 0
	v_add_u32_e32 v36, -1, v2
	v_fma_f32 v37, -v36, v2, v1
	v_cmp_ge_f32_e64 s[40:41], 0, v37
	v_add_u32_e32 v37, 1, v2
	s_nop 0
	v_cndmask_b32_e64 v36, v2, v36, s[40:41]
	v_fma_f32 v2, -v37, v2, v1
	v_cmp_lt_f32_e64 s[40:41], 0, v2
	s_nop 1
	v_cndmask_b32_e64 v2, v36, v37, s[40:41]
	v_mul_f32_e32 v36, 0x37800000, v2
	v_cndmask_b32_e32 v2, v2, v36, vcc
	v_cmp_class_f32_e32 vcc, v1, v241
	s_nop 1
	v_cndmask_b32_e32 v1, v2, v1, vcc
	v_div_scale_f32 v2, s[18:19], v1, v1, 1.0
	v_rcp_f32_e32 v36, v2
	s_nop 0
	v_fma_f32 v37, -v2, v36, 1.0
	v_fmac_f32_e32 v36, v37, v36
	v_div_scale_f32 v37, vcc, 1.0, v1, 1.0
	v_mul_f32_e32 v119, v37, v36
	v_fma_f32 v120, -v2, v119, v37
	v_fmac_f32_e32 v119, v120, v36
	v_fma_f32 v2, -v2, v119, v37
	v_div_fmas_f32 v2, v2, v36, v119
	v_div_fixup_f32 v2, v2, v1, 1.0
	v_lshlrev_b32_e32 v120, 16, v38
	v_lshlrev_b32_e32 v36, 16, v40
	v_and_b32_e32 v37, 0xffff0000, v40
	v_pk_mul_f32 v[120:121], v[2:3], v[120:121] op_sel_hi:[0,1]
	v_lshlrev_b32_e32 v38, 16, v39
	v_and_b32_e32 v39, 0xffff0000, v39
	v_pk_fma_f32 v[36:37], v[4:5], v[120:121], v[36:37]
	v_lshlrev_b32_e32 v40, 16, v41
	v_and_b32_e32 v41, 0xffff0000, v41
	v_pk_mul_f32 v[38:39], v[2:3], v[38:39] op_sel_hi:[0,1]
	v_lshlrev_b32_e32 v120, 16, v42
	v_and_b32_e32 v121, 0xffff0000, v42
	v_pk_fma_f32 v[38:39], v[6:7], v[38:39], v[40:41]
	v_lshlrev_b32_e32 v40, 16, v44
	v_and_b32_e32 v41, 0xffff0000, v44
	v_pk_mul_f32 v[120:121], v[2:3], v[120:121] op_sel_hi:[0,1]
	v_lshlrev_b32_e32 v42, 16, v43
	v_and_b32_e32 v43, 0xffff0000, v43
	v_pk_fma_f32 v[40:41], v[8:9], v[120:121], v[40:41]
	v_lshlrev_b32_e32 v44, 16, v45
	v_and_b32_e32 v45, 0xffff0000, v45
	v_pk_mul_f32 v[42:43], v[2:3], v[42:43] op_sel_hi:[0,1]
	v_lshlrev_b32_e32 v120, 16, v46
	v_and_b32_e32 v121, 0xffff0000, v46
	v_pk_fma_f32 v[42:43], v[10:11], v[42:43], v[44:45]
	v_lshlrev_b32_e32 v44, 16, v48
	v_and_b32_e32 v45, 0xffff0000, v48
	v_pk_mul_f32 v[120:121], v[2:3], v[120:121] op_sel_hi:[0,1]
	v_lshlrev_b32_e32 v46, 16, v47
	v_and_b32_e32 v47, 0xffff0000, v47
	v_pk_fma_f32 v[44:45], v[12:13], v[120:121], v[44:45]
	v_lshlrev_b32_e32 v48, 16, v49
	v_and_b32_e32 v49, 0xffff0000, v49
	v_pk_mul_f32 v[46:47], v[2:3], v[46:47] op_sel_hi:[0,1]
	v_lshlrev_b32_e32 v120, 16, v50
	v_and_b32_e32 v121, 0xffff0000, v50
	v_pk_fma_f32 v[46:47], v[14:15], v[46:47], v[48:49]
	v_lshlrev_b32_e32 v48, 16, v52
	v_and_b32_e32 v49, 0xffff0000, v52
	v_pk_mul_f32 v[120:121], v[2:3], v[120:121] op_sel_hi:[0,1]
	v_lshlrev_b32_e32 v50, 16, v51
	v_and_b32_e32 v51, 0xffff0000, v51
	v_pk_fma_f32 v[48:49], v[16:17], v[120:121], v[48:49]
	v_lshlrev_b32_e32 v52, 16, v53
	v_and_b32_e32 v53, 0xffff0000, v53
	v_pk_mul_f32 v[50:51], v[2:3], v[50:51] op_sel_hi:[0,1]
	v_lshlrev_b32_e32 v120, 16, v54
	v_and_b32_e32 v121, 0xffff0000, v54
	v_pk_fma_f32 v[50:51], v[18:19], v[50:51], v[52:53]
	v_lshlrev_b32_e32 v52, 16, v56
	v_and_b32_e32 v53, 0xffff0000, v56
	v_pk_mul_f32 v[120:121], v[2:3], v[120:121] op_sel_hi:[0,1]
	v_lshlrev_b32_e32 v54, 16, v55
	v_and_b32_e32 v55, 0xffff0000, v55
	v_pk_fma_f32 v[52:53], v[20:21], v[120:121], v[52:53]
	v_lshlrev_b32_e32 v56, 16, v57
	v_and_b32_e32 v57, 0xffff0000, v57
	v_pk_mul_f32 v[54:55], v[2:3], v[54:55] op_sel_hi:[0,1]
	v_lshlrev_b32_e32 v120, 16, v58
	v_and_b32_e32 v121, 0xffff0000, v58
	v_pk_fma_f32 v[54:55], v[22:23], v[54:55], v[56:57]
	v_lshlrev_b32_e32 v56, 16, v60
	v_and_b32_e32 v57, 0xffff0000, v60
	v_pk_mul_f32 v[120:121], v[2:3], v[120:121] op_sel_hi:[0,1]
	v_lshlrev_b32_e32 v58, 16, v59
	v_and_b32_e32 v59, 0xffff0000, v59
	v_pk_fma_f32 v[56:57], v[24:25], v[120:121], v[56:57]
	v_lshlrev_b32_e32 v60, 16, v61
	v_and_b32_e32 v61, 0xffff0000, v61
	v_pk_mul_f32 v[58:59], v[2:3], v[58:59] op_sel_hi:[0,1]
	v_lshlrev_b32_e32 v120, 16, v62
	v_and_b32_e32 v121, 0xffff0000, v62
	v_pk_fma_f32 v[58:59], v[26:27], v[58:59], v[60:61]
	v_lshlrev_b32_e32 v60, 16, v64
	v_and_b32_e32 v61, 0xffff0000, v64
	v_pk_mul_f32 v[120:121], v[2:3], v[120:121] op_sel_hi:[0,1]
	v_lshlrev_b32_e32 v62, 16, v63
	v_and_b32_e32 v63, 0xffff0000, v63
	v_pk_fma_f32 v[60:61], v[28:29], v[120:121], v[60:61]
	v_lshlrev_b32_e32 v64, 16, v65
	v_and_b32_e32 v65, 0xffff0000, v65
	v_pk_mul_f32 v[62:63], v[2:3], v[62:63] op_sel_hi:[0,1]
	v_lshlrev_b32_e32 v120, 16, v66
	v_and_b32_e32 v121, 0xffff0000, v66
	v_lshlrev_b32_e32 v66, 16, v67
	v_and_b32_e32 v67, 0xffff0000, v67
	v_pk_fma_f32 v[62:63], v[30:31], v[62:63], v[64:65]
	v_lshlrev_b32_e32 v64, 16, v110
	v_and_b32_e32 v65, 0xffff0000, v110
	v_pk_mul_f32 v[120:121], v[2:3], v[120:121] op_sel_hi:[0,1]
	v_lshlrev_b32_e32 v110, 16, v111
	v_and_b32_e32 v111, 0xffff0000, v111
	v_pk_mul_f32 v[66:67], v[2:3], v[66:67] op_sel_hi:[0,1]
	v_pk_fma_f32 v[64:65], v[32:33], v[120:121], v[64:65]
	v_pk_fma_f32 v[66:67], v[34:35], v[66:67], v[110:111]
	s_waitcnt vmcnt(0)
	s_andn2_b64 vcc, exec, s[44:45]
	s_cbranch_vccnz .LBB0_1370
	global_store_dwordx4 v[72:73], v[36:39], off offset:-4096
	global_store_dwordx4 v[72:73], v[40:43], off offset:-3072
	global_store_dwordx4 v[72:73], v[44:47], off offset:-2048
	global_store_dwordx4 v[72:73], v[48:51], off offset:-1024
	global_store_dwordx4 v[72:73], v[52:55], off
	global_store_dwordx4 v[72:73], v[56:59], off offset:1024
	global_store_dwordx4 v[72:73], v[60:63], off offset:2048
	global_store_dwordx4 v[72:73], v[64:67], off offset:3072
	s_cbranch_execnz .LBB0_1363
	s_branch .LBB0_1371
